# full-wave sum and max reductions (expert phase token norms, activation absmax, next-layer rstd; prologue) done with DPP row ops + row_bcast + readlane instead of 6 serialized ds_bpermute round trips
# speedup vs baseline: 1.0057x; 1.0057x over previous
; #define GAS __attribute__((address_space(1)))
; __device__ __forceinline__ unsigned f2bf(float f) { unsigned u = __builtin_bit_cast(unsigned, f); return (u + 0x7fffu + ((u >> 16) & 1u)) >> 16; }
; __device__ __forceinline__ void row_to_fp4(const float* src, unsigned char* dst, size_t slice_stride, unsigned short* scale_out, int lane) {
;     f32x4 v[8]; float mx = 0.f;
; #pragma unroll
;     for (int q = 0; q < 8; ++q) { v[q] = ld_f4(src + q * 256 + lane * 4);
;         mx = fmaxf(mx, fmaxf(fmaxf(__builtin_fabsf(v[q][0]), __builtin_fabsf(v[q][1])), fmaxf(__builtin_fabsf(v[q][2]), __builtin_fabsf(v[q][3])))); }
; #pragma unroll
;     for (int o = 1; o < 64; o <<= 1) mx = fmaxf(mx, __shfl_xor(mx, o));
;     const float sc = mx > 0.f ? bf_lo(f2bf(mx * (1.0f / 6.0f)) ) : 1.0f, inv = 1.0f / sc;
; #pragma unroll
;     for (int q = 0; q < 8; ++q) { const f32x4 a = v[q] * inv;
;         unsigned w = 0u;
;         w = __builtin_amdgcn_cvt_scalef32_pk_fp4_f32(w, a[0], a[1], 1.0f, 0); w = __builtin_amdgcn_cvt_scalef32_pk_fp4_f32(w, a[2], a[3], 1.0f, 1);
;         *(GAS unsigned short*)(dst + (size_t)q * slice_stride + lane * 2) = (unsigned short)w; }
;     if (lane == 0) *(GAS unsigned short*)scale_out = (unsigned short)f2bf(sc);
; }
.LBB0_147:
	s_add_i32 s8, s21, 0xffff0000
	s_cmp_gt_i32 s21, 0xffff
	s_cselect_b64 s[2:3], -1, 0
	s_and_b64 s[6:7], s[2:3], exec
	s_cselect_b32 s6, s8, s21
	s_cselect_b32 s22, s59, s57
	s_cselect_b32 s23, s58, s56
	s_ashr_i32 s7, s6, 31
	s_lshl_b64 s[8:9], s[6:7], 13
	s_add_u32 s8, s23, s8
	s_addc_u32 s9, s22, s9
	v_lshl_add_u64 v[0:1], v[34:35], 2, s[8:9]
	global_load_dwordx4 v[28:31], v[0:1], off
	global_load_dwordx4 v[24:27], v[0:1], off offset:1024
	global_load_dwordx4 v[20:23], v[0:1], off offset:2048
	global_load_dwordx4 v[16:19], v[0:1], off offset:3072
	v_add_co_u32_e32 v0, vcc, s12, v0
	s_waitcnt vmcnt(3)
	v_max_f32_e64 v45, |v31|, |v31|
	v_addc_co_u32_e32 v1, vcc, 0, v1, vcc
	s_waitcnt lgkmcnt(0)
	global_load_dwordx4 v[12:15], v[0:1], off
	global_load_dwordx4 v[8:11], v[0:1], off offset:1024
	global_load_dwordx4 v[4:7], v[0:1], off offset:2048
	s_nop 0
	global_load_dwordx4 v[0:3], v[0:1], off offset:3072
	v_max_f32_e64 v46, |v30|, |v30|
	s_waitcnt vmcnt(6)
	v_max_f32_e64 v47, |v27|, |v27|
	v_max_f32_e64 v48, |v26|, |v26|
	s_waitcnt vmcnt(5)
	v_max_f32_e64 v49, |v23|, |v23|
	v_max_f32_e64 v50, |v22|, |v22|
	s_waitcnt vmcnt(4)
	v_max_f32_e64 v51, |v19|, |v19|
	v_max_f32_e64 v52, |v18|, |v18|
	v_max_f32_e32 v45, v46, v45
	v_max_f32_e32 v46, v48, v47
	v_max_f32_e32 v47, v50, v49
	v_max_f32_e32 v48, v52, v51
	v_max3_f32 v45, |v28|, |v29|, v45
	v_max3_f32 v46, |v24|, |v25|, v46
	v_max3_f32 v47, |v20|, |v21|, v47
	v_max3_f32 v48, |v16|, |v17|, v48
	v_max3_f32 v45, v45, 0, v46
	v_max3_f32 v45, v45, v47, v48
	s_waitcnt vmcnt(3)
	v_max_f32_e64 v49, |v15|, |v15|
	v_max_f32_e64 v50, |v14|, |v14|
	s_waitcnt vmcnt(2)
	v_max_f32_e64 v51, |v11|, |v11|
	v_max_f32_e64 v52, |v10|, |v10|
	s_waitcnt vmcnt(1)
	v_max_f32_e64 v53, |v7|, |v7|
	v_max_f32_e64 v54, |v6|, |v6|
	s_waitcnt vmcnt(0)
	v_max_f32_e64 v55, |v3|, |v3|
	v_max_f32_e64 v56, |v2|, |v2|
	v_max_f32_e32 v49, v50, v49
	v_max_f32_e32 v50, v52, v51
	v_max_f32_e32 v51, v54, v53
	v_max_f32_e32 v52, v56, v55
	v_max3_f32 v46, |v12|, |v13|, v49
	v_max3_f32 v49, |v8|, |v9|, v50
	v_max3_f32 v50, |v4|, |v5|, v51
	v_max3_f32 v51, |v0|, |v1|, v52
	v_max3_f32 v45, v45, v46, v49
	v_max3_f32 v45, v45, v50, v51
	s_waitcnt lgkmcnt(0)
	s_nop 1
	v_max_f32_dpp v45, v45, v45 quad_perm:[1,0,3,2] row_mask:0xf bank_mask:0xf
	s_nop 1
	v_max_f32_dpp v45, v45, v45 quad_perm:[2,3,0,1] row_mask:0xf bank_mask:0xf
	s_nop 1
	v_max_f32_dpp v45, v45, v45 row_half_mirror row_mask:0xf bank_mask:0xf
	s_nop 1
	v_max_f32_dpp v45, v45, v45 row_mirror row_mask:0xf bank_mask:0xf
	s_nop 1
	v_max_f32_dpp v45, v45, v45 row_bcast:15 row_mask:0xa bank_mask:0xf
	s_nop 1
	v_max_f32_dpp v45, v45, v45 row_bcast:31 row_mask:0xc bank_mask:0xf
	s_nop 1
	v_readlane_b32 s100, v45, 63
	s_nop 3
	v_mov_b32_e32 v45, s100
	v_mov_b32_e32 v46, s100
	s_waitcnt lgkmcnt(0)
	v_max_f32_e32 v46, v46, v46
	v_max_f32_e32 v46, v45, v46
	v_cmp_lt_f32_e32 vcc, 0, v46
	v_mov_b32_e32 v45, 1.0
	s_and_saveexec_b64 s[8:9], vcc
	v_mul_f32_e32 v45, 0x3e2aaaab, v46
	v_bfe_u32 v46, v45, 16, 1
	v_add3_u32 v45, v45, v46, s13
	v_and_b32_e32 v45, 0xffff0000, v45
	s_or_b64 exec, exec, s[8:9]
	s_and_b64 s[8:9], s[2:3], exec
	s_cselect_b32 s8, s14, 0x3b400000
	s_add_u32 s22, s62, s8
	s_addc_u32 s23, s63, 0
	s_lshr_b32 s8, s7, 18
	s_add_i32 s24, s6, s8
	s_ashr_i32 s8, s24, 14
	s_ashr_i32 s9, s8, 31
	s_lshl_b64 s[8:9], s[8:9], 24
	s_add_u32 s25, s22, s8
	s_addc_u32 s26, s23, s9
	v_div_scale_f32 v46, s[22:23], v45, v45, 1.0
	v_rcp_f32_e32 v47, v46
	s_and_b32 s8, s24, 0xffffc000
	s_sub_i32 s8, s6, s8
	s_ashr_i32 s9, s8, 31
	v_fma_f32 v48, -v46, v47, 1.0
	v_fmac_f32_e32 v47, v48, v47
	v_div_scale_f32 v48, vcc, 1.0, v45, 1.0
	v_mul_f32_e32 v49, v48, v47
	v_fma_f32 v50, -v46, v49, v48
	v_fmac_f32_e32 v49, v50, v47
	v_fma_f32 v46, -v46, v49, v48
	v_div_fmas_f32 v46, v46, v47, v49
	v_div_fixup_f32 v46, v46, v45, 1.0
	s_lshl_b64 s[8:9], s[8:9], 7
	v_pk_mul_f32 v[30:31], v[30:31], v[46:47] op_sel_hi:[1,0]
	v_pk_mul_f32 v[28:29], v[28:29], v[46:47] op_sel_hi:[1,0]
	v_mov_b32_e32 v47, 0
	s_add_u32 s8, s25, s8
	v_cvt_scalef32_pk_fp4_f32 v47, v28, v29, 1.0
	s_addc_u32 s9, s26, s9
	v_cvt_scalef32_pk_fp4_f32 v47, v30, v31, 1.0 op_sel:[0,0,1,0]
	v_lshl_add_u64 v[48:49], s[8:9], 0, v[36:37]
	v_pk_mul_f32 v[24:25], v[24:25], v[46:47] op_sel_hi:[1,0]
	v_mov_b32_e32 v28, 0
	v_pk_mul_f32 v[26:27], v[26:27], v[46:47] op_sel_hi:[1,0]
	v_cvt_scalef32_pk_fp4_f32 v28, v24, v25, 1.0
	v_add_co_u32_e32 v24, vcc, s15, v48
	v_cvt_scalef32_pk_fp4_f32 v28, v26, v27, 1.0 op_sel:[0,0,1,0]
	s_nop 0
	v_addc_co_u32_e32 v25, vcc, 0, v49, vcc
	global_store_short v[24:25], v28, off
	v_pk_mul_f32 v[20:21], v[20:21], v[46:47] op_sel_hi:[1,0]
	v_mov_b32_e32 v24, 0
	v_pk_mul_f32 v[22:23], v[22:23], v[46:47] op_sel_hi:[1,0]
	v_cvt_scalef32_pk_fp4_f32 v24, v20, v21, 1.0
	v_add_co_u32_e32 v20, vcc, s16, v48
	v_cvt_scalef32_pk_fp4_f32 v24, v22, v23, 1.0 op_sel:[0,0,1,0]
	s_nop 0
	v_addc_co_u32_e32 v21, vcc, 0, v49, vcc
	global_store_short v[20:21], v24, off
	v_pk_mul_f32 v[16:17], v[16:17], v[46:47] op_sel_hi:[1,0]
	v_mov_b32_e32 v20, 0
	v_pk_mul_f32 v[18:19], v[18:19], v[46:47] op_sel_hi:[1,0]
	v_cvt_scalef32_pk_fp4_f32 v20, v16, v17, 1.0
	v_add_co_u32_e32 v16, vcc, s17, v48
	v_cvt_scalef32_pk_fp4_f32 v20, v18, v19, 1.0 op_sel:[0,0,1,0]
	s_nop 0
	v_addc_co_u32_e32 v17, vcc, 0, v49, vcc
	global_store_short v[16:17], v20, off
	v_pk_mul_f32 v[12:13], v[12:13], v[46:47] op_sel_hi:[1,0]
	v_mov_b32_e32 v16, 0
	v_pk_mul_f32 v[14:15], v[14:15], v[46:47] op_sel_hi:[1,0]
	v_cvt_scalef32_pk_fp4_f32 v16, v12, v13, 1.0
	v_add_co_u32_e32 v12, vcc, s18, v48
	v_cvt_scalef32_pk_fp4_f32 v16, v14, v15, 1.0 op_sel:[0,0,1,0]
	s_nop 0
	v_addc_co_u32_e32 v13, vcc, 0, v49, vcc
	global_store_short v[12:13], v16, off
	v_pk_mul_f32 v[8:9], v[8:9], v[46:47] op_sel_hi:[1,0]
	v_mov_b32_e32 v12, 0
	v_pk_mul_f32 v[10:11], v[10:11], v[46:47] op_sel_hi:[1,0]
	v_cvt_scalef32_pk_fp4_f32 v12, v8, v9, 1.0
	v_add_co_u32_e32 v8, vcc, s19, v48
	v_cvt_scalef32_pk_fp4_f32 v12, v10, v11, 1.0 op_sel:[0,0,1,0]
	s_nop 0
	v_addc_co_u32_e32 v9, vcc, 0, v49, vcc
	global_store_short v[8:9], v12, off
	v_pk_mul_f32 v[4:5], v[4:5], v[46:47] op_sel_hi:[1,0]
	v_mov_b32_e32 v8, 0
	v_pk_mul_f32 v[6:7], v[6:7], v[46:47] op_sel_hi:[1,0]
	v_cvt_scalef32_pk_fp4_f32 v8, v4, v5, 1.0
	v_add_co_u32_e32 v4, vcc, s20, v48
	v_cvt_scalef32_pk_fp4_f32 v8, v6, v7, 1.0 op_sel:[0,0,1,0]
	s_nop 0
	v_addc_co_u32_e32 v5, vcc, 0, v49, vcc
	global_store_short v[4:5], v8, off
	v_pk_mul_f32 v[0:1], v[0:1], v[46:47] op_sel_hi:[1,0]
	v_mov_b32_e32 v4, 0
	v_pk_mul_f32 v[2:3], v[2:3], v[46:47] op_sel_hi:[1,0]
	v_cvt_scalef32_pk_fp4_f32 v4, v0, v1, 1.0
	v_add_co_u32_e32 v0, vcc, 0xe00000, v48
	v_cvt_scalef32_pk_fp4_f32 v4, v2, v3, 1.0 op_sel:[0,0,1,0]
	s_nop 0
	v_addc_co_u32_e32 v1, vcc, 0, v49, vcc
	global_store_short v[48:49], v47, off
	global_store_short v[0:1], v4, off
	s_and_saveexec_b64 s[8:9], s[0:1]
	s_cbranch_execz .LBB0_146
; #define GAS __attribute__((address_space(1)))
; __device__ __forceinline__ unsigned f2bf(float f) { unsigned u = __builtin_bit_cast(unsigned, f); return (u + 0x7fffu + ((u >> 16) & 1u)) >> 16; }
; __device__ __forceinline__ void row_to_fp4(const float* src, unsigned char* dst, size_t slice_stride, unsigned short* scale_out, int lane) {
;     ...
;     if (lane == 0) *(GAS unsigned short*)scale_out = (unsigned short)f2bf(sc);
	s_lshl_b64 s[6:7], s[6:7], 2
	s_add_u32 s6, s10, s6
	v_cndmask_b32_e64 v0, 0, 1, s[2:3]
	v_bfe_u32 v1, v45, 16, 1
	s_addc_u32 s7, s11, s7
	v_lshlrev_b32_e32 v0, 1, v0
	v_add3_u32 v1, v45, v1, s13
	global_store_short_d16_hi v0, v1, s[6:7]
	s_branch .LBB0_146

; #define GAS __attribute__((address_space(1)))
; #define LAS __attribute__((address_space(3)))
; __device__ __forceinline__ float frsq(float x) { return __builtin_amdgcn_rsqf(x); }
; __device__ __forceinline__ void expert_phase(const Frame& F, int l, int xcc, LAS unsigned char* wl, const LAS unsigned char* zb) {
;     ...
;             float zf = 0.f; asm volatile("" : "+v"(zf)); const f32x4 z = (f32x4){zf, zf, zf, zf};
; #pragma unroll
;             for (int i = 0; i < 8; ++i) *(LAS f32x4*)(SA + (i * 64 + lane) * 4) = z;
; #pragma unroll
;             for (int i = 0; i < 2; ++i) *(LAS f32x4*)(SQ + (i * 64 + lane) * 4) = z;
; #pragma unroll
;             for (int k = 0; k < 8; ++k) { const u32x2 e2 = ldo_u2(EXPI + (size_t)tok(k) * 128, 8u * lane); *(LAS unsigned*)(IDL + k * 256 + lane * 4) = e2.x | (e2.y << 16); }
;             const float* SS2 = (const float*)(F.ws + WS_SS2);
;             float ss[8];
; #pragma unroll
;             for (int k = 0; k < 8; ++k) ss[k] = *(const GAS float*)(SS2 + (size_t)(lane & 31) * T + tok(k));
; #pragma unroll
;             for (int k = 0; k < 8; ++k) { const float tot = wave_sum(ss[k]) * 0.5f; if (lane == 0) RS[k] = frsq(tot * (1.f / D) + EPS); }
.LBB0_1125:
	v_mov_b32_e32 v0, v185
	s_ashr_i32 s27, s26, 31
	v_add_u32_e32 v4, s83, v182
	s_waitcnt lgkmcnt(0)
	v_mov_b32_e32 v1, v0
	v_mov_b32_e32 v2, v0
	v_mov_b32_e32 v3, v0
	s_lshl_b64 s[2:3], s[26:27], 9
	ds_write_b128 v4, v[0:3]
	ds_write_b128 v4, v[0:3] offset:1024
	ds_write_b128 v4, v[0:3] offset:2048
	ds_write_b128 v4, v[0:3] offset:3072
	ds_write_b128 v4, v[0:3] offset:4096
	ds_write_b128 v4, v[0:3] offset:5120
	ds_write_b128 v4, v[0:3] offset:6144
	ds_write_b128 v4, v[0:3] offset:7168
	ds_write_b128 v4, v[0:3] offset:8192
	ds_write_b128 v4, v[0:3] offset:9216
	v_lshl_add_u64 v[0:1], v[168:169], 0, s[2:3]
	global_load_dwordx2 v[10:11], v[0:1], off
	s_add_i32 s0, s26, s82
	s_cmpk_lt_i32 s0, 0x4000
	s_cselect_b32 s88, s0, s26
	s_ashr_i32 s89, s88, 31
	s_lshl_b64 s[86:87], s[88:89], 9
	s_add_i32 s4, s0, s82
	s_cmpk_lt_i32 s4, 0x4000
	s_cselect_b32 s0, s4, s26
	s_ashr_i32 s1, s0, 31
	v_add_u32_e32 v3, 64, v201
	s_lshl_b64 s[68:69], s[0:1], 9
	s_add_i32 s4, s4, s82
	s_cmpk_lt_i32 s4, 0x4000
	s_cselect_b32 s16, s4, s26
	s_ashr_i32 s17, s16, 31
	s_lshl_b64 s[80:81], s[16:17], 9
	s_add_i32 s4, s4, s82
	s_cmpk_lt_i32 s4, 0x4000
	s_cselect_b32 s14, s4, s26
	s_ashr_i32 s15, s14, 31
	s_lshl_b64 s[8:9], s[14:15], 9
	s_add_i32 s4, s4, s82
	s_cmpk_lt_i32 s4, 0x4000
	s_cselect_b32 s12, s4, s26
	s_ashr_i32 s13, s12, 31
	s_lshl_b64 s[66:67], s[12:13], 9
	s_add_i32 s4, s4, s82
	s_cmpk_lt_i32 s4, 0x4000
	s_cselect_b32 s94, s4, s26
	s_ashr_i32 s95, s94, 31
	s_lshl_b64 s[30:31], s[94:95], 9
	s_add_i32 s4, s4, s82
	s_cmpk_lt_i32 s4, 0x4000
	s_cselect_b32 s6, s4, s26
	s_ashr_i32 s7, s6, 31
	s_lshl_b64 s[44:45], s[6:7], 9
	v_lshl_add_u64 v[8:9], s[6:7], 2, v[166:167]
	v_lshl_add_u64 v[0:1], v[168:169], 0, s[86:87]
	global_load_dwordx2 v[12:13], v[0:1], off
	v_lshl_add_u64 v[0:1], v[168:169], 0, s[68:69]
	global_load_dwordx2 v[14:15], v[0:1], off
	v_lshl_add_u64 v[0:1], v[168:169], 0, s[80:81]
	global_load_dwordx2 v[16:17], v[0:1], off
	v_lshl_add_u64 v[0:1], v[168:169], 0, s[8:9]
	global_load_dwordx2 v[18:19], v[0:1], off
	v_lshl_add_u64 v[0:1], v[168:169], 0, s[66:67]
	global_load_dwordx2 v[20:21], v[0:1], off
	v_lshl_add_u64 v[0:1], v[168:169], 0, s[30:31]
	global_load_dwordx2 v[22:23], v[0:1], off
	v_lshl_add_u64 v[0:1], v[168:169], 0, s[44:45]
	global_load_dwordx2 v[24:25], v[0:1], off
	s_waitcnt vmcnt(0)
	v_lshl_or_b32 v2, v11, 16, v10
	v_lshl_or_b32 v0, v13, 16, v12
	ds_write2st64_b32 v3, v2, v0 offset0:42 offset1:43
	v_lshl_or_b32 v2, v15, 16, v14
	v_lshl_or_b32 v0, v17, 16, v16
	ds_write2st64_b32 v3, v2, v0 offset0:44 offset1:45
	v_lshl_or_b32 v2, v19, 16, v18
	v_lshl_or_b32 v0, v21, 16, v20
	ds_write2st64_b32 v3, v2, v0 offset0:46 offset1:47
	v_lshl_or_b32 v2, v23, 16, v22
	v_lshl_or_b32 v0, v25, 16, v24
	ds_write2st64_b32 v3, v2, v0 offset0:48 offset1:49
	v_lshl_add_u64 v[0:1], s[26:27], 2, v[166:167]
	global_load_dword v7, v[0:1], off
	v_lshl_add_u64 v[0:1], s[88:89], 2, v[166:167]
	global_load_dword v6, v[0:1], off
	v_lshl_add_u64 v[0:1], s[0:1], 2, v[166:167]
	global_load_dword v5, v[0:1], off
	v_lshl_add_u64 v[0:1], s[16:17], 2, v[166:167]
	global_load_dword v4, v[0:1], off
	v_lshl_add_u64 v[0:1], s[14:15], 2, v[166:167]
	global_load_dword v3, v[0:1], off
	v_lshl_add_u64 v[0:1], s[12:13], 2, v[166:167]
	global_load_dword v2, v[0:1], off
	v_lshl_add_u64 v[0:1], s[94:95], 2, v[166:167]
	global_load_dword v1, v[0:1], off
	s_nop 0
	global_load_dword v0, v[8:9], off
	s_waitcnt vmcnt(7)
	s_waitcnt lgkmcnt(0)
	s_nop 1
	v_add_f32_dpp v7, v7, v7 quad_perm:[1,0,3,2] row_mask:0xf bank_mask:0xf
	s_nop 1
	v_add_f32_dpp v7, v7, v7 quad_perm:[2,3,0,1] row_mask:0xf bank_mask:0xf
	s_nop 1
	v_add_f32_dpp v7, v7, v7 row_half_mirror row_mask:0xf bank_mask:0xf
	s_nop 1
	v_add_f32_dpp v7, v7, v7 row_mirror row_mask:0xf bank_mask:0xf
	s_nop 1
	v_add_f32_dpp v7, v7, v7 row_bcast:15 row_mask:0xa bank_mask:0xf
	s_nop 1
	v_add_f32_dpp v7, v7, v7 row_bcast:31 row_mask:0xc bank_mask:0xf
	s_nop 1
	v_readlane_b32 s100, v7, 63
	s_nop 3
	v_mov_b32_e32 v7, s100
	v_mov_b32_e32 v8, 0
	s_and_saveexec_b64 s[64:65], s[34:35]
	s_cbranch_execz .LBB0_1127
	s_waitcnt lgkmcnt(0)
	v_add_f32_e32 v7, v7, v8
	v_mul_f32_e32 v7, 0.5, v7
	v_fmamk_f32 v7, v7, 0x3a000000, v214
	v_rsq_f32_e32 v7, v7
	v_mov_b32_e32 v8, s83
	ds_write_b32 v8, v7 offset:10240
.LBB0_1127:
	s_or_b64 exec, exec, s[64:65]
	s_waitcnt vmcnt(6)
	s_waitcnt lgkmcnt(0)
	s_nop 1
	v_add_f32_dpp v6, v6, v6 quad_perm:[1,0,3,2] row_mask:0xf bank_mask:0xf
	s_nop 1
	v_add_f32_dpp v6, v6, v6 quad_perm:[2,3,0,1] row_mask:0xf bank_mask:0xf
	s_nop 1
	v_add_f32_dpp v6, v6, v6 row_half_mirror row_mask:0xf bank_mask:0xf
	s_nop 1
	v_add_f32_dpp v6, v6, v6 row_mirror row_mask:0xf bank_mask:0xf
	s_nop 1
	v_add_f32_dpp v6, v6, v6 row_bcast:15 row_mask:0xa bank_mask:0xf
	s_nop 1
	v_add_f32_dpp v6, v6, v6 row_bcast:31 row_mask:0xc bank_mask:0xf
	s_nop 1
	v_readlane_b32 s100, v6, 63
	s_nop 3
	v_mov_b32_e32 v6, s100
	v_mov_b32_e32 v7, 0
	s_and_saveexec_b64 s[64:65], s[34:35]
	s_cbranch_execz .LBB0_1129
	s_waitcnt lgkmcnt(0)
	v_add_f32_e32 v6, v6, v7
	v_mul_f32_e32 v6, 0.5, v6
	v_fmamk_f32 v6, v6, 0x3a000000, v214
	v_rsq_f32_e32 v6, v6
	v_mov_b32_e32 v7, s83
	ds_write_b32 v7, v6 offset:10244
; #define GAS __attribute__((address_space(1)))
; __device__ __forceinline__ float frsq(float x) { return __builtin_amdgcn_rsqf(x); }
; __device__ __forceinline__ void expert_phase(const Frame& F, int l, int xcc, LAS unsigned char* wl, const LAS unsigned char* zb) {
;     ...
;             for (int k = 0; k < 8; ++k) ss[k] = *(const GAS float*)(SS2 + (size_t)(lane & 31) * T + tok(k));
; #pragma unroll
;             for (int k = 0; k < 8; ++k) { const float tot = wave_sum(ss[k]) * 0.5f; if (lane == 0) RS[k] = frsq(tot * (1.f / D) + EPS); }
.LBB0_1129:
	s_or_b64 exec, exec, s[64:65]
	s_waitcnt vmcnt(5)
	s_waitcnt lgkmcnt(0)
	s_nop 1
	v_add_f32_dpp v5, v5, v5 quad_perm:[1,0,3,2] row_mask:0xf bank_mask:0xf
	s_nop 1
	v_add_f32_dpp v5, v5, v5 quad_perm:[2,3,0,1] row_mask:0xf bank_mask:0xf
	s_nop 1
	v_add_f32_dpp v5, v5, v5 row_half_mirror row_mask:0xf bank_mask:0xf
	s_nop 1
	v_add_f32_dpp v5, v5, v5 row_mirror row_mask:0xf bank_mask:0xf
	s_nop 1
	v_add_f32_dpp v5, v5, v5 row_bcast:15 row_mask:0xa bank_mask:0xf
	s_nop 1
	v_add_f32_dpp v5, v5, v5 row_bcast:31 row_mask:0xc bank_mask:0xf
	s_nop 1
	v_readlane_b32 s100, v5, 63
	s_nop 3
	v_mov_b32_e32 v5, s100
	v_mov_b32_e32 v6, 0
	s_and_saveexec_b64 s[64:65], s[34:35]
	s_cbranch_execz .LBB0_1131
	s_waitcnt lgkmcnt(0)
	v_add_f32_e32 v5, v5, v6
	v_mul_f32_e32 v5, 0.5, v5
	v_fmamk_f32 v5, v5, 0x3a000000, v214
	v_rsq_f32_e32 v5, v5
	v_mov_b32_e32 v6, s83
	ds_write_b32 v6, v5 offset:10248
.LBB0_1131:
	s_or_b64 exec, exec, s[64:65]
	s_waitcnt vmcnt(4)
	s_waitcnt lgkmcnt(0)
	s_nop 1
	v_add_f32_dpp v4, v4, v4 quad_perm:[1,0,3,2] row_mask:0xf bank_mask:0xf
	s_nop 1
	v_add_f32_dpp v4, v4, v4 quad_perm:[2,3,0,1] row_mask:0xf bank_mask:0xf
	s_nop 1
	v_add_f32_dpp v4, v4, v4 row_half_mirror row_mask:0xf bank_mask:0xf
	s_nop 1
	v_add_f32_dpp v4, v4, v4 row_mirror row_mask:0xf bank_mask:0xf
	s_nop 1
	v_add_f32_dpp v4, v4, v4 row_bcast:15 row_mask:0xa bank_mask:0xf
	s_nop 1
	v_add_f32_dpp v4, v4, v4 row_bcast:31 row_mask:0xc bank_mask:0xf
	s_nop 1
	v_readlane_b32 s100, v4, 63
	s_nop 3
	v_mov_b32_e32 v4, s100
	v_mov_b32_e32 v5, 0
	s_and_saveexec_b64 s[64:65], s[34:35]
	s_cbranch_execz .LBB0_1133
	s_waitcnt lgkmcnt(0)
	v_add_f32_e32 v4, v4, v5
	v_mul_f32_e32 v4, 0.5, v4
	v_fmamk_f32 v4, v4, 0x3a000000, v214
	v_rsq_f32_e32 v4, v4
	v_mov_b32_e32 v5, s83
	ds_write_b32 v5, v4 offset:10252
.LBB0_1133:
	s_or_b64 exec, exec, s[64:65]
	s_waitcnt vmcnt(3)
	s_waitcnt lgkmcnt(0)
	s_nop 1
	v_add_f32_dpp v3, v3, v3 quad_perm:[1,0,3,2] row_mask:0xf bank_mask:0xf
	s_nop 1
	v_add_f32_dpp v3, v3, v3 quad_perm:[2,3,0,1] row_mask:0xf bank_mask:0xf
	s_nop 1
	v_add_f32_dpp v3, v3, v3 row_half_mirror row_mask:0xf bank_mask:0xf
	s_nop 1
	v_add_f32_dpp v3, v3, v3 row_mirror row_mask:0xf bank_mask:0xf
	s_nop 1
	v_add_f32_dpp v3, v3, v3 row_bcast:15 row_mask:0xa bank_mask:0xf
	s_nop 1
	v_add_f32_dpp v3, v3, v3 row_bcast:31 row_mask:0xc bank_mask:0xf
	s_nop 1
	v_readlane_b32 s100, v3, 63
	s_nop 3
	v_mov_b32_e32 v3, s100
	v_mov_b32_e32 v4, 0
	s_and_saveexec_b64 s[64:65], s[34:35]
	s_cbranch_execz .LBB0_1135
	s_waitcnt lgkmcnt(0)
	v_add_f32_e32 v3, v3, v4
	v_mul_f32_e32 v3, 0.5, v3
	v_fmamk_f32 v3, v3, 0x3a000000, v214
	v_rsq_f32_e32 v3, v3
	v_mov_b32_e32 v4, s83
	ds_write_b32 v4, v3 offset:10256
.LBB0_1135:
	s_or_b64 exec, exec, s[64:65]
	s_waitcnt vmcnt(2)
	s_waitcnt lgkmcnt(0)
	s_nop 1
	v_add_f32_dpp v2, v2, v2 quad_perm:[1,0,3,2] row_mask:0xf bank_mask:0xf
	s_nop 1
	v_add_f32_dpp v2, v2, v2 quad_perm:[2,3,0,1] row_mask:0xf bank_mask:0xf
	s_nop 1
	v_add_f32_dpp v2, v2, v2 row_half_mirror row_mask:0xf bank_mask:0xf
	s_nop 1
	v_add_f32_dpp v2, v2, v2 row_mirror row_mask:0xf bank_mask:0xf
	s_nop 1
	v_add_f32_dpp v2, v2, v2 row_bcast:15 row_mask:0xa bank_mask:0xf
	s_nop 1
	v_add_f32_dpp v2, v2, v2 row_bcast:31 row_mask:0xc bank_mask:0xf
	s_nop 1
	v_readlane_b32 s100, v2, 63
	s_nop 3
	v_mov_b32_e32 v2, s100
	v_mov_b32_e32 v3, 0
	s_and_saveexec_b64 s[64:65], s[34:35]
	s_cbranch_execz .LBB0_1137
	s_waitcnt lgkmcnt(0)
	v_add_f32_e32 v2, v2, v3
	v_mul_f32_e32 v2, 0.5, v2
	v_fmamk_f32 v2, v2, 0x3a000000, v214
	v_rsq_f32_e32 v2, v2
	v_mov_b32_e32 v3, s83
	ds_write_b32 v3, v2 offset:10260
.LBB0_1137:
	s_or_b64 exec, exec, s[64:65]
	s_waitcnt vmcnt(1)
	s_waitcnt lgkmcnt(0)
	s_nop 1
	v_add_f32_dpp v1, v1, v1 quad_perm:[1,0,3,2] row_mask:0xf bank_mask:0xf
	s_nop 1
	v_add_f32_dpp v1, v1, v1 quad_perm:[2,3,0,1] row_mask:0xf bank_mask:0xf
	s_nop 1
	v_add_f32_dpp v1, v1, v1 row_half_mirror row_mask:0xf bank_mask:0xf
	s_nop 1
	v_add_f32_dpp v1, v1, v1 row_mirror row_mask:0xf bank_mask:0xf
	s_nop 1
	v_add_f32_dpp v1, v1, v1 row_bcast:15 row_mask:0xa bank_mask:0xf
	s_nop 1
	v_add_f32_dpp v1, v1, v1 row_bcast:31 row_mask:0xc bank_mask:0xf
	s_nop 1
	v_readlane_b32 s100, v1, 63
	s_nop 3
	v_mov_b32_e32 v1, s100
	v_mov_b32_e32 v2, 0
	s_and_saveexec_b64 s[64:65], s[34:35]
	s_cbranch_execz .LBB0_1139
	s_waitcnt lgkmcnt(0)
	v_add_f32_e32 v1, v1, v2
	v_mul_f32_e32 v1, 0.5, v1
	v_fmamk_f32 v1, v1, 0x3a000000, v214
	v_rsq_f32_e32 v1, v1
	v_mov_b32_e32 v2, s83
	ds_write_b32 v2, v1 offset:10264
.LBB0_1139:
	s_or_b64 exec, exec, s[64:65]
	s_waitcnt vmcnt(0)
	s_waitcnt lgkmcnt(0)
	s_nop 1
	v_add_f32_dpp v0, v0, v0 quad_perm:[1,0,3,2] row_mask:0xf bank_mask:0xf
	s_nop 1
	v_add_f32_dpp v0, v0, v0 quad_perm:[2,3,0,1] row_mask:0xf bank_mask:0xf
	s_nop 1
	v_add_f32_dpp v0, v0, v0 row_half_mirror row_mask:0xf bank_mask:0xf
	s_nop 1
	v_add_f32_dpp v0, v0, v0 row_mirror row_mask:0xf bank_mask:0xf
	s_nop 1
	v_add_f32_dpp v0, v0, v0 row_bcast:15 row_mask:0xa bank_mask:0xf
	s_nop 1
	v_add_f32_dpp v0, v0, v0 row_bcast:31 row_mask:0xc bank_mask:0xf
	s_nop 1
	v_readlane_b32 s100, v0, 63
	s_nop 3
	v_mov_b32_e32 v0, s100
	v_mov_b32_e32 v1, 0
	s_and_saveexec_b64 s[64:65], s[34:35]
	s_cbranch_execz .LBB0_1141
	s_waitcnt lgkmcnt(0)
	v_add_f32_e32 v0, v0, v1
	v_mul_f32_e32 v0, 0.5, v0
	v_fmamk_f32 v0, v0, 0x3a000000, v214
	v_rsq_f32_e32 v0, v0
	v_mov_b32_e32 v1, s83
	ds_write_b32 v1, v0 offset:10268

; #define LAS __attribute__((address_space(3)))
; #define XFENCE() asm volatile("" ::: "memory")
; __device__ __forceinline__ void expert_phase(const Frame& F, int l, int xcc, LAS unsigned char* wl, const LAS unsigned char* zb) {
;     ...
;                 for (int hf = 0; hf < 2; ++hf) {
;                     const unsigned suv = suvq[k][hf];
;                     const int kk = hf * 64 + lane;
;                     const float a = (SA[k * 256 + (kk & 7) * 32 + (kk >> 3)] + SA[k * 256 + (kk & 7) * 32 + 16 + (kk >> 3)]) * bf_lo(suv);
;                     wq[hf] = gtq[k][hf] * bf_hi(suv) * 0.5f * a * (1.0f + erff(a * 0.7071067811865476f));
;                 }
;                 XFENCE();
;                 float wm = fmaxf(__builtin_fabsf(wq[0]), __builtin_fabsf(wq[1]));
; #pragma unroll
;                 for (int o = 1; o < 64; o <<= 1) wm = fmaxf(wm, __shfl_xor(wm, o));
;                 const float sc = __builtin_bit_cast(float, __builtin_bit_cast(unsigned, fminf(42.0f / fmaxf(wm, 1e-30f), 1.0e18f)) & 0x7f800000u);
;                 const unsigned h0 = (unsigned)__builtin_bit_cast(unsigned short, (_Float16)(wq[0] * sc)), h1 = (unsigned)__builtin_bit_cast(unsigned short, (_Float16)(wq[1] * sc));
;                 ((LAS unsigned*)SA)[k * 256 + lane] = h0 | (h0 << 16); ((LAS unsigned*)SA)[k * 256 + 64 + lane] = h1 | (h1 << 16);
;                 if (lane == 0) RS[8 + k] = 1.0f / sc;
.LBB0_1165:
	s_andn2_saveexec_b64 s[2:3], s[2:3]
	v_mul_f32_e32 v37, v36, v36
	v_fmamk_f32 v38, v37, 0xba1345e1, v216
	v_fmaak_f32 v38, v37, v38, 0xbcdac9b8
	v_fmaak_f32 v38, v37, v38, 0x3de703be
	v_fmaak_f32 v38, v37, v38, 0xbec09330
	v_fmaak_f32 v37, v37, v38, 0x3e0375d0
	v_fma_f32 v37, |v36|, v37, |v36|
	s_or_b64 exec, exec, s[2:3]
	v_and_b32_e32 v30, 0xffff0000, v30
	v_and_b32_e32 v12, 0xffff0000, v12
	v_mul_f32_e32 v30, v31, v30
	s_waitcnt vmcnt(28)
	v_mul_f32_e32 v12, v29, v12
	v_mul_f32_e32 v30, 0.5, v30
	v_bfi_b32 v31, s58, v34, v33
	v_mul_f32_e32 v12, 0.5, v12
	v_bfi_b32 v29, s58, v37, v36
	v_mul_f32_e32 v30, v30, v32
	v_add_f32_e32 v31, 1.0, v31
	v_mul_f32_e32 v12, v12, v35
	v_add_f32_e32 v29, 1.0, v29
	v_mul_f32_e32 v30, v30, v31
	v_mul_f32_e32 v31, v12, v29
	v_max_f32_e64 v12, |v30|, |v31|
	s_waitcnt lgkmcnt(0)
	s_nop 1
	v_max_f32_dpp v12, v12, v12 quad_perm:[1,0,3,2] row_mask:0xf bank_mask:0xf
	s_nop 1
	v_max_f32_dpp v12, v12, v12 quad_perm:[2,3,0,1] row_mask:0xf bank_mask:0xf
	s_nop 1
	v_max_f32_dpp v12, v12, v12 row_half_mirror row_mask:0xf bank_mask:0xf
	s_nop 1
	v_max_f32_dpp v12, v12, v12 row_mirror row_mask:0xf bank_mask:0xf
	s_nop 1
	v_max_f32_dpp v12, v12, v12 row_bcast:15 row_mask:0xa bank_mask:0xf
	s_nop 1
	v_max_f32_dpp v12, v12, v12 row_bcast:31 row_mask:0xc bank_mask:0xf
	s_nop 1
	v_readlane_b32 s100, v12, 63
	s_nop 3
	v_mov_b32_e32 v12, s100
	v_mov_b32_e32 v29, s100
	s_waitcnt lgkmcnt(0)
	v_max3_f32 v29, v12, v29, s64
	v_div_scale_f32 v32, s[2:3], v29, v29, s65
	v_rcp_f32_e32 v33, v32
	v_div_scale_f32 v34, vcc, s65, v29, s65
	v_add_u32_e32 v12, v203, v183
	v_fma_f32 v35, -v32, v33, 1.0
	v_fmac_f32_e32 v33, v35, v33
	v_mul_f32_e32 v35, v34, v33
	v_fma_f32 v36, -v32, v35, v34
	v_fmac_f32_e32 v35, v36, v33
	v_fma_f32 v32, -v32, v35, v34
	v_div_fmas_f32 v32, v32, v33, v35
	v_div_fixup_f32 v29, v32, v29, s65
	v_min_f32_e32 v29, 0x5d5e0b6b, v29
	v_and_b32_e32 v29, 0x7f800000, v29
	v_fma_mixlo_f16 v30, v30, v29, 0
	v_fma_mixlo_f16 v31, v31, v29, 0
	v_mul_u32_u24_sdwa v30, v30, s66 dst_sel:DWORD dst_unused:UNUSED_PAD src0_sel:WORD_0 src1_sel:DWORD
	v_mul_u32_u24_sdwa v31, v31, s66 dst_sel:DWORD dst_unused:UNUSED_PAD src0_sel:WORD_0 src1_sel:DWORD
	ds_write2st64_b32 v12, v30, v31 offset1:1
	s_and_saveexec_b64 s[2:3], s[34:35]
	s_cbranch_execz .LBB0_1169
	v_div_scale_f32 v30, s[4:5], v29, v29, 1.0
	v_rcp_f32_e32 v31, v30
	v_div_scale_f32 v32, vcc, 1.0, v29, 1.0
	v_fma_f32 v33, -v30, v31, 1.0
	v_fmac_f32_e32 v31, v33, v31
	v_mul_f32_e32 v33, v32, v31
	v_fma_f32 v34, -v30, v33, v32
	v_fmac_f32_e32 v33, v34, v31
	v_fma_f32 v30, -v30, v33, v32
	v_div_fmas_f32 v30, v30, v31, v33
	v_div_fixup_f32 v29, v30, v29, 1.0
	v_mov_b32_e32 v30, s83
	ds_write_b32 v30, v29 offset:10272

; #define LAS __attribute__((address_space(3)))
; #define XFENCE() asm volatile("" ::: "memory")
; __device__ __forceinline__ void expert_phase(const Frame& F, int l, int xcc, LAS unsigned char* wl, const LAS unsigned char* zb) {
;     ...
;                 for (int hf = 0; hf < 2; ++hf) {
;                     const unsigned suv = suvq[k][hf];
;                     const int kk = hf * 64 + lane;
;                     const float a = (SA[k * 256 + (kk & 7) * 32 + (kk >> 3)] + SA[k * 256 + (kk & 7) * 32 + 16 + (kk >> 3)]) * bf_lo(suv);
;                     wq[hf] = gtq[k][hf] * bf_hi(suv) * 0.5f * a * (1.0f + erff(a * 0.7071067811865476f));
;                 }
;                 XFENCE();
;                 float wm = fmaxf(__builtin_fabsf(wq[0]), __builtin_fabsf(wq[1]));
; #pragma unroll
;                 for (int o = 1; o < 64; o <<= 1) wm = fmaxf(wm, __shfl_xor(wm, o));
;                 const float sc = __builtin_bit_cast(float, __builtin_bit_cast(unsigned, fminf(42.0f / fmaxf(wm, 1e-30f), 1.0e18f)) & 0x7f800000u);
;                 const unsigned h0 = (unsigned)__builtin_bit_cast(unsigned short, (_Float16)(wq[0] * sc)), h1 = (unsigned)__builtin_bit_cast(unsigned short, (_Float16)(wq[1] * sc));
;                 ((LAS unsigned*)SA)[k * 256 + lane] = h0 | (h0 << 16); ((LAS unsigned*)SA)[k * 256 + 64 + lane] = h1 | (h1 << 16);
;                 if (lane == 0) RS[8 + k] = 1.0f / sc;
.LBB0_1175:
	s_andn2_saveexec_b64 s[2:3], s[2:3]
	v_mul_f32_e32 v34, v33, v33
	v_fmamk_f32 v35, v34, 0xba1345e1, v216
	v_fmaak_f32 v35, v34, v35, 0xbcdac9b8
	v_fmaak_f32 v35, v34, v35, 0x3de703be
	v_fmaak_f32 v35, v34, v35, 0xbec09330
	v_fmaak_f32 v34, v34, v35, 0x3e0375d0
	v_fma_f32 v34, |v33|, v34, |v33|
	s_or_b64 exec, exec, s[2:3]
	v_and_b32_e32 v27, 0xffff0000, v27
	v_and_b32_e32 v25, 0xffff0000, v25
	v_mul_f32_e32 v27, v28, v27
	s_waitcnt vmcnt(24)
	v_mul_f32_e32 v25, v26, v25
	v_mul_f32_e32 v27, 0.5, v27
	v_bfi_b32 v28, s58, v31, v30
	v_mul_f32_e32 v25, 0.5, v25
	v_bfi_b32 v26, s58, v34, v33
	v_mul_f32_e32 v27, v27, v29
	v_add_f32_e32 v28, 1.0, v28
	v_mul_f32_e32 v25, v25, v32
	v_add_f32_e32 v26, 1.0, v26
	v_mul_f32_e32 v27, v27, v28
	v_mul_f32_e32 v26, v25, v26
	v_max_f32_e64 v25, |v27|, |v26|
	s_waitcnt lgkmcnt(0)
	s_nop 1
	v_max_f32_dpp v25, v25, v25 quad_perm:[1,0,3,2] row_mask:0xf bank_mask:0xf
	s_nop 1
	v_max_f32_dpp v25, v25, v25 quad_perm:[2,3,0,1] row_mask:0xf bank_mask:0xf
	s_nop 1
	v_max_f32_dpp v25, v25, v25 row_half_mirror row_mask:0xf bank_mask:0xf
	s_nop 1
	v_max_f32_dpp v25, v25, v25 row_mirror row_mask:0xf bank_mask:0xf
	s_nop 1
	v_max_f32_dpp v25, v25, v25 row_bcast:15 row_mask:0xa bank_mask:0xf
	s_nop 1
	v_max_f32_dpp v25, v25, v25 row_bcast:31 row_mask:0xc bank_mask:0xf
	s_nop 1
	v_readlane_b32 s100, v25, 63
	s_nop 3
	v_mov_b32_e32 v25, s100
	v_mov_b32_e32 v28, s100
	s_waitcnt lgkmcnt(0)
	v_max3_f32 v25, v25, v28, s64
	v_div_scale_f32 v28, s[2:3], v25, v25, s65
	v_rcp_f32_e32 v29, v28
	v_div_scale_f32 v30, vcc, s65, v25, s65
	v_fma_f32 v31, -v28, v29, 1.0
	v_fmac_f32_e32 v29, v31, v29
	v_mul_f32_e32 v31, v30, v29
	v_fma_f32 v32, -v28, v31, v30
	v_fmac_f32_e32 v31, v32, v29
	v_fma_f32 v28, -v28, v31, v30
	v_div_fmas_f32 v28, v28, v29, v31
	v_div_fixup_f32 v25, v28, v25, s65
	v_min_f32_e32 v25, 0x5d5e0b6b, v25
	v_and_b32_e32 v25, 0x7f800000, v25
	v_fma_mixlo_f16 v27, v27, v25, 0
	v_fma_mixlo_f16 v26, v26, v25, 0
	v_mul_u32_u24_sdwa v27, v27, s66 dst_sel:DWORD dst_unused:UNUSED_PAD src0_sel:WORD_0 src1_sel:DWORD
	v_mul_u32_u24_sdwa v26, v26, s66 dst_sel:DWORD dst_unused:UNUSED_PAD src0_sel:WORD_0 src1_sel:DWORD
	ds_write2st64_b32 v12, v27, v26 offset0:4 offset1:5
	s_and_saveexec_b64 s[2:3], s[34:35]
	s_cbranch_execz .LBB0_1179
	v_div_scale_f32 v26, s[4:5], v25, v25, 1.0
	v_rcp_f32_e32 v27, v26
	v_div_scale_f32 v28, vcc, 1.0, v25, 1.0
	v_fma_f32 v29, -v26, v27, 1.0
	v_fmac_f32_e32 v27, v29, v27
	v_mul_f32_e32 v29, v28, v27
	v_fma_f32 v30, -v26, v29, v28
	v_fmac_f32_e32 v29, v30, v27
	v_fma_f32 v26, -v26, v29, v28
	v_div_fmas_f32 v26, v26, v27, v29
	v_div_fixup_f32 v25, v26, v25, 1.0
	v_mov_b32_e32 v26, s83
	ds_write_b32 v26, v25 offset:10276

; #define LAS __attribute__((address_space(3)))
; #define XFENCE() asm volatile("" ::: "memory")
; __device__ __forceinline__ void expert_phase(const Frame& F, int l, int xcc, LAS unsigned char* wl, const LAS unsigned char* zb) {
;     ...
;                 for (int hf = 0; hf < 2; ++hf) {
;                     const unsigned suv = suvq[k][hf];
;                     const int kk = hf * 64 + lane;
;                     const float a = (SA[k * 256 + (kk & 7) * 32 + (kk >> 3)] + SA[k * 256 + (kk & 7) * 32 + 16 + (kk >> 3)]) * bf_lo(suv);
;                     wq[hf] = gtq[k][hf] * bf_hi(suv) * 0.5f * a * (1.0f + erff(a * 0.7071067811865476f));
;                 }
;                 XFENCE();
;                 float wm = fmaxf(__builtin_fabsf(wq[0]), __builtin_fabsf(wq[1]));
; #pragma unroll
;                 for (int o = 1; o < 64; o <<= 1) wm = fmaxf(wm, __shfl_xor(wm, o));
;                 const float sc = __builtin_bit_cast(float, __builtin_bit_cast(unsigned, fminf(42.0f / fmaxf(wm, 1e-30f), 1.0e18f)) & 0x7f800000u);
;                 const unsigned h0 = (unsigned)__builtin_bit_cast(unsigned short, (_Float16)(wq[0] * sc)), h1 = (unsigned)__builtin_bit_cast(unsigned short, (_Float16)(wq[1] * sc));
;                 ((LAS unsigned*)SA)[k * 256 + lane] = h0 | (h0 << 16); ((LAS unsigned*)SA)[k * 256 + 64 + lane] = h1 | (h1 << 16);
;                 if (lane == 0) RS[8 + k] = 1.0f / sc;
.LBB0_1185:
	s_andn2_saveexec_b64 s[2:3], s[2:3]
	v_mul_f32_e32 v30, v29, v29
	v_fmamk_f32 v31, v30, 0xba1345e1, v216
	v_fmaak_f32 v31, v30, v31, 0xbcdac9b8
	v_fmaak_f32 v31, v30, v31, 0x3de703be
	v_fmaak_f32 v31, v30, v31, 0xbec09330
	v_fmaak_f32 v30, v30, v31, 0x3e0375d0
	v_fma_f32 v30, |v29|, v30, |v29|
	s_or_b64 exec, exec, s[2:3]
	v_and_b32_e32 v23, 0xffff0000, v23
	v_and_b32_e32 v21, 0xffff0000, v21
	v_mul_f32_e32 v23, v24, v23
	s_waitcnt vmcnt(20)
	v_mul_f32_e32 v21, v22, v21
	v_mul_f32_e32 v23, 0.5, v23
	v_bfi_b32 v24, s58, v27, v26
	v_mul_f32_e32 v21, 0.5, v21
	v_bfi_b32 v22, s58, v30, v29
	v_mul_f32_e32 v23, v23, v25
	v_add_f32_e32 v24, 1.0, v24
	v_mul_f32_e32 v21, v21, v28
	v_add_f32_e32 v22, 1.0, v22
	v_mul_f32_e32 v23, v23, v24
	v_mul_f32_e32 v22, v21, v22
	v_max_f32_e64 v21, |v23|, |v22|
	s_waitcnt lgkmcnt(0)
	s_nop 1
	v_max_f32_dpp v21, v21, v21 quad_perm:[1,0,3,2] row_mask:0xf bank_mask:0xf
	s_nop 1
	v_max_f32_dpp v21, v21, v21 quad_perm:[2,3,0,1] row_mask:0xf bank_mask:0xf
	s_nop 1
	v_max_f32_dpp v21, v21, v21 row_half_mirror row_mask:0xf bank_mask:0xf
	s_nop 1
	v_max_f32_dpp v21, v21, v21 row_mirror row_mask:0xf bank_mask:0xf
	s_nop 1
	v_max_f32_dpp v21, v21, v21 row_bcast:15 row_mask:0xa bank_mask:0xf
	s_nop 1
	v_max_f32_dpp v21, v21, v21 row_bcast:31 row_mask:0xc bank_mask:0xf
	s_nop 1
	v_readlane_b32 s100, v21, 63
	s_nop 3
	v_mov_b32_e32 v21, s100
	v_mov_b32_e32 v24, s100
	s_waitcnt lgkmcnt(0)
	v_max3_f32 v21, v21, v24, s64
	v_div_scale_f32 v24, s[2:3], v21, v21, s65
	v_rcp_f32_e32 v25, v24
	v_div_scale_f32 v26, vcc, s65, v21, s65
	v_fma_f32 v27, -v24, v25, 1.0
	v_fmac_f32_e32 v25, v27, v25
	v_mul_f32_e32 v27, v26, v25
	v_fma_f32 v28, -v24, v27, v26
	v_fmac_f32_e32 v27, v28, v25
	v_fma_f32 v24, -v24, v27, v26
	v_div_fmas_f32 v24, v24, v25, v27
	v_div_fixup_f32 v21, v24, v21, s65
	v_min_f32_e32 v21, 0x5d5e0b6b, v21
	v_and_b32_e32 v21, 0x7f800000, v21
	v_fma_mixlo_f16 v23, v23, v21, 0
	v_fma_mixlo_f16 v22, v22, v21, 0
	v_mul_u32_u24_sdwa v23, v23, s66 dst_sel:DWORD dst_unused:UNUSED_PAD src0_sel:WORD_0 src1_sel:DWORD
	v_mul_u32_u24_sdwa v22, v22, s66 dst_sel:DWORD dst_unused:UNUSED_PAD src0_sel:WORD_0 src1_sel:DWORD
	ds_write2st64_b32 v12, v23, v22 offset0:8 offset1:9
	s_and_saveexec_b64 s[2:3], s[34:35]
	s_cbranch_execz .LBB0_1189
	v_div_scale_f32 v22, s[4:5], v21, v21, 1.0
	v_rcp_f32_e32 v23, v22
	v_div_scale_f32 v24, vcc, 1.0, v21, 1.0
	v_fma_f32 v25, -v22, v23, 1.0
	v_fmac_f32_e32 v23, v25, v23
	v_mul_f32_e32 v25, v24, v23
	v_fma_f32 v26, -v22, v25, v24
	v_fmac_f32_e32 v25, v26, v23
	v_fma_f32 v22, -v22, v25, v24
	v_div_fmas_f32 v22, v22, v23, v25
	v_div_fixup_f32 v21, v22, v21, 1.0
	v_mov_b32_e32 v22, s83
	ds_write_b32 v22, v21 offset:10280

; #define LAS __attribute__((address_space(3)))
; #define XFENCE() asm volatile("" ::: "memory")
; __device__ __forceinline__ void expert_phase(const Frame& F, int l, int xcc, LAS unsigned char* wl, const LAS unsigned char* zb) {
;     ...
;                 for (int hf = 0; hf < 2; ++hf) {
;                     const unsigned suv = suvq[k][hf];
;                     const int kk = hf * 64 + lane;
;                     const float a = (SA[k * 256 + (kk & 7) * 32 + (kk >> 3)] + SA[k * 256 + (kk & 7) * 32 + 16 + (kk >> 3)]) * bf_lo(suv);
;                     wq[hf] = gtq[k][hf] * bf_hi(suv) * 0.5f * a * (1.0f + erff(a * 0.7071067811865476f));
;                 }
;                 XFENCE();
;                 float wm = fmaxf(__builtin_fabsf(wq[0]), __builtin_fabsf(wq[1]));
; #pragma unroll
;                 for (int o = 1; o < 64; o <<= 1) wm = fmaxf(wm, __shfl_xor(wm, o));
;                 const float sc = __builtin_bit_cast(float, __builtin_bit_cast(unsigned, fminf(42.0f / fmaxf(wm, 1e-30f), 1.0e18f)) & 0x7f800000u);
;                 const unsigned h0 = (unsigned)__builtin_bit_cast(unsigned short, (_Float16)(wq[0] * sc)), h1 = (unsigned)__builtin_bit_cast(unsigned short, (_Float16)(wq[1] * sc));
;                 ((LAS unsigned*)SA)[k * 256 + lane] = h0 | (h0 << 16); ((LAS unsigned*)SA)[k * 256 + 64 + lane] = h1 | (h1 << 16);
;                 if (lane == 0) RS[8 + k] = 1.0f / sc;
.LBB0_1195:
	s_andn2_saveexec_b64 s[2:3], s[2:3]
	v_mul_f32_e32 v26, v25, v25
	v_fmamk_f32 v27, v26, 0xba1345e1, v216
	v_fmaak_f32 v27, v26, v27, 0xbcdac9b8
	v_fmaak_f32 v27, v26, v27, 0x3de703be
	v_fmaak_f32 v27, v26, v27, 0xbec09330
	v_fmaak_f32 v26, v26, v27, 0x3e0375d0
	v_fma_f32 v26, |v25|, v26, |v25|
	s_or_b64 exec, exec, s[2:3]
	v_and_b32_e32 v19, 0xffff0000, v19
	v_and_b32_e32 v17, 0xffff0000, v17
	v_mul_f32_e32 v19, v20, v19
	s_waitcnt vmcnt(16)
	v_mul_f32_e32 v17, v18, v17
	v_mul_f32_e32 v19, 0.5, v19
	v_bfi_b32 v20, s58, v23, v22
	v_mul_f32_e32 v17, 0.5, v17
	v_bfi_b32 v18, s58, v26, v25
	v_mul_f32_e32 v19, v19, v21
	v_add_f32_e32 v20, 1.0, v20
	v_mul_f32_e32 v17, v17, v24
	v_add_f32_e32 v18, 1.0, v18
	v_mul_f32_e32 v19, v19, v20
	v_mul_f32_e32 v18, v17, v18
	v_max_f32_e64 v17, |v19|, |v18|
	s_waitcnt lgkmcnt(0)
	s_nop 1
	v_max_f32_dpp v17, v17, v17 quad_perm:[1,0,3,2] row_mask:0xf bank_mask:0xf
	s_nop 1
	v_max_f32_dpp v17, v17, v17 quad_perm:[2,3,0,1] row_mask:0xf bank_mask:0xf
	s_nop 1
	v_max_f32_dpp v17, v17, v17 row_half_mirror row_mask:0xf bank_mask:0xf
	s_nop 1
	v_max_f32_dpp v17, v17, v17 row_mirror row_mask:0xf bank_mask:0xf
	s_nop 1
	v_max_f32_dpp v17, v17, v17 row_bcast:15 row_mask:0xa bank_mask:0xf
	s_nop 1
	v_max_f32_dpp v17, v17, v17 row_bcast:31 row_mask:0xc bank_mask:0xf
	s_nop 1
	v_readlane_b32 s100, v17, 63
	s_nop 3
	v_mov_b32_e32 v17, s100
	v_mov_b32_e32 v20, s100
	s_waitcnt lgkmcnt(0)
	v_max3_f32 v17, v17, v20, s64
	v_div_scale_f32 v20, s[2:3], v17, v17, s65
	v_rcp_f32_e32 v21, v20
	v_div_scale_f32 v22, vcc, s65, v17, s65
	v_fma_f32 v23, -v20, v21, 1.0
	v_fmac_f32_e32 v21, v23, v21
	v_mul_f32_e32 v23, v22, v21
	v_fma_f32 v24, -v20, v23, v22
	v_fmac_f32_e32 v23, v24, v21
	v_fma_f32 v20, -v20, v23, v22
	v_div_fmas_f32 v20, v20, v21, v23
	v_div_fixup_f32 v17, v20, v17, s65
	v_min_f32_e32 v17, 0x5d5e0b6b, v17
	v_and_b32_e32 v17, 0x7f800000, v17
	v_fma_mixlo_f16 v19, v19, v17, 0
	v_fma_mixlo_f16 v18, v18, v17, 0
	v_mul_u32_u24_sdwa v19, v19, s66 dst_sel:DWORD dst_unused:UNUSED_PAD src0_sel:WORD_0 src1_sel:DWORD
	v_mul_u32_u24_sdwa v18, v18, s66 dst_sel:DWORD dst_unused:UNUSED_PAD src0_sel:WORD_0 src1_sel:DWORD
	ds_write2st64_b32 v12, v19, v18 offset0:12 offset1:13
	s_and_saveexec_b64 s[2:3], s[34:35]
	s_cbranch_execz .LBB0_1199
	v_div_scale_f32 v18, s[4:5], v17, v17, 1.0
	v_rcp_f32_e32 v19, v18
	v_div_scale_f32 v20, vcc, 1.0, v17, 1.0
	v_fma_f32 v21, -v18, v19, 1.0
	v_fmac_f32_e32 v19, v21, v19
	v_mul_f32_e32 v21, v20, v19
	v_fma_f32 v22, -v18, v21, v20
	v_fmac_f32_e32 v21, v22, v19
	v_fma_f32 v18, -v18, v21, v20
	v_div_fmas_f32 v18, v18, v19, v21
	v_div_fixup_f32 v17, v18, v17, 1.0
	v_mov_b32_e32 v18, s83
	ds_write_b32 v18, v17 offset:10284

; #define LAS __attribute__((address_space(3)))
; #define XFENCE() asm volatile("" ::: "memory")
; __device__ __forceinline__ void expert_phase(const Frame& F, int l, int xcc, LAS unsigned char* wl, const LAS unsigned char* zb) {
;     ...
;                 for (int hf = 0; hf < 2; ++hf) {
;                     const unsigned suv = suvq[k][hf];
;                     const int kk = hf * 64 + lane;
;                     const float a = (SA[k * 256 + (kk & 7) * 32 + (kk >> 3)] + SA[k * 256 + (kk & 7) * 32 + 16 + (kk >> 3)]) * bf_lo(suv);
;                     wq[hf] = gtq[k][hf] * bf_hi(suv) * 0.5f * a * (1.0f + erff(a * 0.7071067811865476f));
;                 }
;                 XFENCE();
;                 float wm = fmaxf(__builtin_fabsf(wq[0]), __builtin_fabsf(wq[1]));
; #pragma unroll
;                 for (int o = 1; o < 64; o <<= 1) wm = fmaxf(wm, __shfl_xor(wm, o));
;                 const float sc = __builtin_bit_cast(float, __builtin_bit_cast(unsigned, fminf(42.0f / fmaxf(wm, 1e-30f), 1.0e18f)) & 0x7f800000u);
;                 const unsigned h0 = (unsigned)__builtin_bit_cast(unsigned short, (_Float16)(wq[0] * sc)), h1 = (unsigned)__builtin_bit_cast(unsigned short, (_Float16)(wq[1] * sc));
;                 ((LAS unsigned*)SA)[k * 256 + lane] = h0 | (h0 << 16); ((LAS unsigned*)SA)[k * 256 + 64 + lane] = h1 | (h1 << 16);
;                 if (lane == 0) RS[8 + k] = 1.0f / sc;
.LBB0_1205:
	s_andn2_saveexec_b64 s[2:3], s[2:3]
	v_mul_f32_e32 v22, v21, v21
	v_fmamk_f32 v23, v22, 0xba1345e1, v216
	v_fmaak_f32 v23, v22, v23, 0xbcdac9b8
	v_fmaak_f32 v23, v22, v23, 0x3de703be
	v_fmaak_f32 v23, v22, v23, 0xbec09330
	v_fmaak_f32 v22, v22, v23, 0x3e0375d0
	v_fma_f32 v22, |v21|, v22, |v21|
	s_or_b64 exec, exec, s[2:3]
	v_and_b32_e32 v15, 0xffff0000, v15
	v_and_b32_e32 v13, 0xffff0000, v13
	v_mul_f32_e32 v15, v16, v15
	s_waitcnt vmcnt(12)
	v_mul_f32_e32 v13, v14, v13
	v_mul_f32_e32 v15, 0.5, v15
	v_bfi_b32 v16, s58, v19, v18
	v_mul_f32_e32 v13, 0.5, v13
	v_bfi_b32 v14, s58, v22, v21
	v_mul_f32_e32 v15, v15, v17
	v_add_f32_e32 v16, 1.0, v16
	v_mul_f32_e32 v13, v13, v20
	v_add_f32_e32 v14, 1.0, v14
	v_mul_f32_e32 v15, v15, v16
	v_mul_f32_e32 v14, v13, v14
	v_max_f32_e64 v13, |v15|, |v14|
	s_waitcnt lgkmcnt(0)
	s_nop 1
	v_max_f32_dpp v13, v13, v13 quad_perm:[1,0,3,2] row_mask:0xf bank_mask:0xf
	s_nop 1
	v_max_f32_dpp v13, v13, v13 quad_perm:[2,3,0,1] row_mask:0xf bank_mask:0xf
	s_nop 1
	v_max_f32_dpp v13, v13, v13 row_half_mirror row_mask:0xf bank_mask:0xf
	s_nop 1
	v_max_f32_dpp v13, v13, v13 row_mirror row_mask:0xf bank_mask:0xf
	s_nop 1
	v_max_f32_dpp v13, v13, v13 row_bcast:15 row_mask:0xa bank_mask:0xf
	s_nop 1
	v_max_f32_dpp v13, v13, v13 row_bcast:31 row_mask:0xc bank_mask:0xf
	s_nop 1
	v_readlane_b32 s100, v13, 63
	s_nop 3
	v_mov_b32_e32 v13, s100
	v_mov_b32_e32 v16, s100
	s_waitcnt lgkmcnt(0)
	v_max3_f32 v13, v13, v16, s64
	v_div_scale_f32 v16, s[2:3], v13, v13, s65
	v_rcp_f32_e32 v17, v16
	v_div_scale_f32 v18, vcc, s65, v13, s65
	v_fma_f32 v19, -v16, v17, 1.0
	v_fmac_f32_e32 v17, v19, v17
	v_mul_f32_e32 v19, v18, v17
	v_fma_f32 v20, -v16, v19, v18
	v_fmac_f32_e32 v19, v20, v17
	v_fma_f32 v16, -v16, v19, v18
	v_div_fmas_f32 v16, v16, v17, v19
	v_div_fixup_f32 v13, v16, v13, s65
	v_min_f32_e32 v13, 0x5d5e0b6b, v13
	v_and_b32_e32 v13, 0x7f800000, v13
	v_fma_mixlo_f16 v15, v15, v13, 0
	v_fma_mixlo_f16 v14, v14, v13, 0
	v_mul_u32_u24_sdwa v15, v15, s66 dst_sel:DWORD dst_unused:UNUSED_PAD src0_sel:WORD_0 src1_sel:DWORD
	v_mul_u32_u24_sdwa v14, v14, s66 dst_sel:DWORD dst_unused:UNUSED_PAD src0_sel:WORD_0 src1_sel:DWORD
	ds_write2st64_b32 v12, v15, v14 offset0:16 offset1:17
	s_and_saveexec_b64 s[2:3], s[34:35]
	s_cbranch_execz .LBB0_1209
	v_div_scale_f32 v14, s[4:5], v13, v13, 1.0
	v_rcp_f32_e32 v15, v14
	v_div_scale_f32 v16, vcc, 1.0, v13, 1.0
	v_fma_f32 v17, -v14, v15, 1.0
	v_fmac_f32_e32 v15, v17, v15
	v_mul_f32_e32 v17, v16, v15
	v_fma_f32 v18, -v14, v17, v16
	v_fmac_f32_e32 v17, v18, v15
	v_fma_f32 v14, -v14, v17, v16
	v_div_fmas_f32 v14, v14, v15, v17
	v_div_fixup_f32 v13, v14, v13, 1.0
	v_mov_b32_e32 v14, s83
	ds_write_b32 v14, v13 offset:10288

; #define LAS __attribute__((address_space(3)))
; #define XFENCE() asm volatile("" ::: "memory")
; __device__ __forceinline__ void expert_phase(const Frame& F, int l, int xcc, LAS unsigned char* wl, const LAS unsigned char* zb) {
;     ...
;                 for (int hf = 0; hf < 2; ++hf) {
;                     const unsigned suv = suvq[k][hf];
;                     const int kk = hf * 64 + lane;
;                     const float a = (SA[k * 256 + (kk & 7) * 32 + (kk >> 3)] + SA[k * 256 + (kk & 7) * 32 + 16 + (kk >> 3)]) * bf_lo(suv);
;                     wq[hf] = gtq[k][hf] * bf_hi(suv) * 0.5f * a * (1.0f + erff(a * 0.7071067811865476f));
;                 }
;                 XFENCE();
;                 float wm = fmaxf(__builtin_fabsf(wq[0]), __builtin_fabsf(wq[1]));
; #pragma unroll
;                 for (int o = 1; o < 64; o <<= 1) wm = fmaxf(wm, __shfl_xor(wm, o));
;                 const float sc = __builtin_bit_cast(float, __builtin_bit_cast(unsigned, fminf(42.0f / fmaxf(wm, 1e-30f), 1.0e18f)) & 0x7f800000u);
;                 const unsigned h0 = (unsigned)__builtin_bit_cast(unsigned short, (_Float16)(wq[0] * sc)), h1 = (unsigned)__builtin_bit_cast(unsigned short, (_Float16)(wq[1] * sc));
;                 ((LAS unsigned*)SA)[k * 256 + lane] = h0 | (h0 << 16); ((LAS unsigned*)SA)[k * 256 + 64 + lane] = h1 | (h1 << 16);
;                 if (lane == 0) RS[8 + k] = 1.0f / sc;
.LBB0_1215:
	s_andn2_saveexec_b64 s[2:3], s[2:3]
	v_mul_f32_e32 v18, v17, v17
	v_fmamk_f32 v19, v18, 0xba1345e1, v216
	v_fmaak_f32 v19, v18, v19, 0xbcdac9b8
	v_fmaak_f32 v19, v18, v19, 0x3de703be
	v_fmaak_f32 v19, v18, v19, 0xbec09330
	v_fmaak_f32 v18, v18, v19, 0x3e0375d0
	v_fma_f32 v18, |v17|, v18, |v17|
	s_or_b64 exec, exec, s[2:3]
	v_and_b32_e32 v10, 0xffff0000, v10
	v_and_b32_e32 v8, 0xffff0000, v8
	v_mul_f32_e32 v10, v11, v10
	s_waitcnt vmcnt(8)
	v_mul_f32_e32 v8, v9, v8
	v_mul_f32_e32 v10, 0.5, v10
	v_bfi_b32 v11, s58, v15, v14
	v_mul_f32_e32 v8, 0.5, v8
	v_bfi_b32 v9, s58, v18, v17
	v_mul_f32_e32 v10, v10, v13
	v_add_f32_e32 v11, 1.0, v11
	v_mul_f32_e32 v8, v8, v16
	v_add_f32_e32 v9, 1.0, v9
	v_mul_f32_e32 v10, v10, v11
	v_mul_f32_e32 v9, v8, v9
	v_max_f32_e64 v8, |v10|, |v9|
	s_waitcnt lgkmcnt(0)
	s_nop 1
	v_max_f32_dpp v8, v8, v8 quad_perm:[1,0,3,2] row_mask:0xf bank_mask:0xf
	s_nop 1
	v_max_f32_dpp v8, v8, v8 quad_perm:[2,3,0,1] row_mask:0xf bank_mask:0xf
	s_nop 1
	v_max_f32_dpp v8, v8, v8 row_half_mirror row_mask:0xf bank_mask:0xf
	s_nop 1
	v_max_f32_dpp v8, v8, v8 row_mirror row_mask:0xf bank_mask:0xf
	s_nop 1
	v_max_f32_dpp v8, v8, v8 row_bcast:15 row_mask:0xa bank_mask:0xf
	s_nop 1
	v_max_f32_dpp v8, v8, v8 row_bcast:31 row_mask:0xc bank_mask:0xf
	s_nop 1
	v_readlane_b32 s100, v8, 63
	s_nop 3
	v_mov_b32_e32 v8, s100
	v_mov_b32_e32 v11, s100
	s_waitcnt lgkmcnt(0)
	v_max3_f32 v8, v8, v11, s64
	v_div_scale_f32 v11, s[2:3], v8, v8, s65
	v_rcp_f32_e32 v13, v11
	v_div_scale_f32 v14, vcc, s65, v8, s65
	v_fma_f32 v15, -v11, v13, 1.0
	v_fmac_f32_e32 v13, v15, v13
	v_mul_f32_e32 v15, v14, v13
	v_fma_f32 v16, -v11, v15, v14
	v_fmac_f32_e32 v15, v16, v13
	v_fma_f32 v11, -v11, v15, v14
	v_div_fmas_f32 v11, v11, v13, v15
	v_div_fixup_f32 v8, v11, v8, s65
	v_min_f32_e32 v8, 0x5d5e0b6b, v8
	v_and_b32_e32 v8, 0x7f800000, v8
	v_fma_mixlo_f16 v10, v10, v8, 0
	v_fma_mixlo_f16 v9, v9, v8, 0
	v_mul_u32_u24_sdwa v10, v10, s66 dst_sel:DWORD dst_unused:UNUSED_PAD src0_sel:WORD_0 src1_sel:DWORD
	v_mul_u32_u24_sdwa v9, v9, s66 dst_sel:DWORD dst_unused:UNUSED_PAD src0_sel:WORD_0 src1_sel:DWORD
	ds_write2st64_b32 v12, v10, v9 offset0:20 offset1:21
	s_and_saveexec_b64 s[2:3], s[34:35]
	s_cbranch_execz .LBB0_1219
	v_div_scale_f32 v9, s[4:5], v8, v8, 1.0
	v_rcp_f32_e32 v10, v9
	v_div_scale_f32 v11, vcc, 1.0, v8, 1.0
	v_fma_f32 v13, -v9, v10, 1.0
	v_fmac_f32_e32 v10, v13, v10
	v_mul_f32_e32 v13, v11, v10
	v_fma_f32 v14, -v9, v13, v11
	v_fmac_f32_e32 v13, v14, v10
	v_fma_f32 v9, -v9, v13, v11
	v_div_fmas_f32 v9, v9, v10, v13
	v_div_fixup_f32 v8, v9, v8, 1.0
	v_mov_b32_e32 v9, s83
	ds_write_b32 v9, v8 offset:10292

; #define LAS __attribute__((address_space(3)))
; #define XFENCE() asm volatile("" ::: "memory")
; __device__ __forceinline__ void expert_phase(const Frame& F, int l, int xcc, LAS unsigned char* wl, const LAS unsigned char* zb) {
;     ...
;                 for (int hf = 0; hf < 2; ++hf) {
;                     const unsigned suv = suvq[k][hf];
;                     const int kk = hf * 64 + lane;
;                     const float a = (SA[k * 256 + (kk & 7) * 32 + (kk >> 3)] + SA[k * 256 + (kk & 7) * 32 + 16 + (kk >> 3)]) * bf_lo(suv);
;                     wq[hf] = gtq[k][hf] * bf_hi(suv) * 0.5f * a * (1.0f + erff(a * 0.7071067811865476f));
;                 }
;                 XFENCE();
;                 float wm = fmaxf(__builtin_fabsf(wq[0]), __builtin_fabsf(wq[1]));
; #pragma unroll
;                 for (int o = 1; o < 64; o <<= 1) wm = fmaxf(wm, __shfl_xor(wm, o));
;                 const float sc = __builtin_bit_cast(float, __builtin_bit_cast(unsigned, fminf(42.0f / fmaxf(wm, 1e-30f), 1.0e18f)) & 0x7f800000u);
;                 const unsigned h0 = (unsigned)__builtin_bit_cast(unsigned short, (_Float16)(wq[0] * sc)), h1 = (unsigned)__builtin_bit_cast(unsigned short, (_Float16)(wq[1] * sc));
;                 ((LAS unsigned*)SA)[k * 256 + lane] = h0 | (h0 << 16); ((LAS unsigned*)SA)[k * 256 + 64 + lane] = h1 | (h1 << 16);
;                 if (lane == 0) RS[8 + k] = 1.0f / sc;
.LBB0_1225:
	s_andn2_saveexec_b64 s[2:3], s[2:3]
	v_mul_f32_e32 v14, v13, v13
	v_fmamk_f32 v15, v14, 0xba1345e1, v216
	v_fmaak_f32 v15, v14, v15, 0xbcdac9b8
	v_fmaak_f32 v15, v14, v15, 0x3de703be
	v_fmaak_f32 v15, v14, v15, 0xbec09330
	v_fmaak_f32 v14, v14, v15, 0x3e0375d0
	v_fma_f32 v14, |v13|, v14, |v13|
	s_or_b64 exec, exec, s[2:3]
	v_and_b32_e32 v4, 0xffff0000, v4
	v_and_b32_e32 v2, 0xffff0000, v2
	v_mul_f32_e32 v4, v5, v4
	s_waitcnt vmcnt(4)
	v_mul_f32_e32 v2, v3, v2
	v_mul_f32_e32 v4, 0.5, v4
	v_bfi_b32 v5, s58, v10, v9
	v_mul_f32_e32 v2, 0.5, v2
	v_bfi_b32 v3, s58, v14, v13
	v_mul_f32_e32 v4, v4, v8
	v_add_f32_e32 v5, 1.0, v5
	v_mul_f32_e32 v2, v2, v11
	v_add_f32_e32 v3, 1.0, v3
	v_mul_f32_e32 v4, v4, v5
	v_mul_f32_e32 v3, v2, v3
	v_max_f32_e64 v2, |v4|, |v3|
	s_waitcnt lgkmcnt(0)
	s_nop 1
	v_max_f32_dpp v2, v2, v2 quad_perm:[1,0,3,2] row_mask:0xf bank_mask:0xf
	s_nop 1
	v_max_f32_dpp v2, v2, v2 quad_perm:[2,3,0,1] row_mask:0xf bank_mask:0xf
	s_nop 1
	v_max_f32_dpp v2, v2, v2 row_half_mirror row_mask:0xf bank_mask:0xf
	s_nop 1
	v_max_f32_dpp v2, v2, v2 row_mirror row_mask:0xf bank_mask:0xf
	s_nop 1
	v_max_f32_dpp v2, v2, v2 row_bcast:15 row_mask:0xa bank_mask:0xf
	s_nop 1
	v_max_f32_dpp v2, v2, v2 row_bcast:31 row_mask:0xc bank_mask:0xf
	s_nop 1
	v_readlane_b32 s100, v2, 63
	s_nop 3
	v_mov_b32_e32 v2, s100
	v_mov_b32_e32 v5, s100
	s_waitcnt lgkmcnt(0)
	v_max3_f32 v2, v2, v5, s64
	v_div_scale_f32 v5, s[2:3], v2, v2, s65
	v_rcp_f32_e32 v8, v5
	v_div_scale_f32 v9, vcc, s65, v2, s65
	v_fma_f32 v10, -v5, v8, 1.0
	v_fmac_f32_e32 v8, v10, v8
	v_mul_f32_e32 v10, v9, v8
	v_fma_f32 v11, -v5, v10, v9
	v_fmac_f32_e32 v10, v11, v8
	v_fma_f32 v5, -v5, v10, v9
	v_div_fmas_f32 v5, v5, v8, v10
	v_div_fixup_f32 v2, v5, v2, s65
	v_min_f32_e32 v2, 0x5d5e0b6b, v2
	v_and_b32_e32 v2, 0x7f800000, v2
	v_fma_mixlo_f16 v4, v4, v2, 0
	v_fma_mixlo_f16 v3, v3, v2, 0
	v_mul_u32_u24_sdwa v4, v4, s66 dst_sel:DWORD dst_unused:UNUSED_PAD src0_sel:WORD_0 src1_sel:DWORD
	v_mul_u32_u24_sdwa v3, v3, s66 dst_sel:DWORD dst_unused:UNUSED_PAD src0_sel:WORD_0 src1_sel:DWORD
	ds_write2st64_b32 v12, v4, v3 offset0:24 offset1:25
	s_and_saveexec_b64 s[2:3], s[34:35]
	s_cbranch_execz .LBB0_1229
	v_div_scale_f32 v3, s[4:5], v2, v2, 1.0
	v_rcp_f32_e32 v4, v3
	v_div_scale_f32 v5, vcc, 1.0, v2, 1.0
	v_fma_f32 v8, -v3, v4, 1.0
	v_fmac_f32_e32 v4, v8, v4
	v_mul_f32_e32 v8, v5, v4
	v_fma_f32 v9, -v3, v8, v5
	v_fmac_f32_e32 v8, v9, v4
	v_fma_f32 v3, -v3, v8, v5
	v_div_fmas_f32 v3, v3, v4, v8
	v_div_fixup_f32 v2, v3, v2, 1.0
	v_mov_b32_e32 v3, s83
	ds_write_b32 v3, v2 offset:10296

; #define LAS __attribute__((address_space(3)))
; #define XFENCE() asm volatile("" ::: "memory")
; __device__ __forceinline__ void expert_phase(const Frame& F, int l, int xcc, LAS unsigned char* wl, const LAS unsigned char* zb) {
;     ...
;                 for (int hf = 0; hf < 2; ++hf) {
;                     const unsigned suv = suvq[k][hf];
;                     const int kk = hf * 64 + lane;
;                     const float a = (SA[k * 256 + (kk & 7) * 32 + (kk >> 3)] + SA[k * 256 + (kk & 7) * 32 + 16 + (kk >> 3)]) * bf_lo(suv);
;                     wq[hf] = gtq[k][hf] * bf_hi(suv) * 0.5f * a * (1.0f + erff(a * 0.7071067811865476f));
;                 }
;                 XFENCE();
;                 float wm = fmaxf(__builtin_fabsf(wq[0]), __builtin_fabsf(wq[1]));
; #pragma unroll
;                 for (int o = 1; o < 64; o <<= 1) wm = fmaxf(wm, __shfl_xor(wm, o));
;                 const float sc = __builtin_bit_cast(float, __builtin_bit_cast(unsigned, fminf(42.0f / fmaxf(wm, 1e-30f), 1.0e18f)) & 0x7f800000u);
;                 const unsigned h0 = (unsigned)__builtin_bit_cast(unsigned short, (_Float16)(wq[0] * sc)), h1 = (unsigned)__builtin_bit_cast(unsigned short, (_Float16)(wq[1] * sc));
;                 ((LAS unsigned*)SA)[k * 256 + lane] = h0 | (h0 << 16); ((LAS unsigned*)SA)[k * 256 + 64 + lane] = h1 | (h1 << 16);
;                 if (lane == 0) RS[8 + k] = 1.0f / sc;
.LBB0_1235:
	s_andn2_saveexec_b64 s[2:3], s[2:3]
	v_mul_f32_e32 v9, v5, v5
	v_fmamk_f32 v10, v9, 0xba1345e1, v216
	v_fmaak_f32 v10, v9, v10, 0xbcdac9b8
	v_fmaak_f32 v10, v9, v10, 0x3de703be
	v_fmaak_f32 v10, v9, v10, 0xbec09330
	v_fmaak_f32 v9, v9, v10, 0x3e0375d0
	v_fma_f32 v9, |v5|, v9, |v5|
	s_or_b64 exec, exec, s[2:3]
	v_and_b32_e32 v0, 0xffff0000, v0
	v_mul_f32_e32 v0, v1, v0
	v_mul_f32_e32 v0, 0.5, v0
	v_bfi_b32 v1, s58, v4, v3
	v_mul_f32_e32 v0, v0, v2
	v_add_f32_e32 v1, 1.0, v1
	v_mul_f32_e32 v1, v0, v1
	v_and_b32_e32 v0, 0xffff0000, v6
	s_waitcnt vmcnt(0)
	v_mul_f32_e32 v0, v7, v0
	v_mul_f32_e32 v0, 0.5, v0
	v_bfi_b32 v2, s58, v9, v5
	v_mul_f32_e32 v0, v0, v8
	v_add_f32_e32 v2, 1.0, v2
	v_mul_f32_e32 v2, v0, v2
	v_max_f32_e64 v0, |v1|, |v2|
	s_waitcnt lgkmcnt(0)
	s_nop 1
	v_max_f32_dpp v0, v0, v0 quad_perm:[1,0,3,2] row_mask:0xf bank_mask:0xf
	s_nop 1
	v_max_f32_dpp v0, v0, v0 quad_perm:[2,3,0,1] row_mask:0xf bank_mask:0xf
	s_nop 1
	v_max_f32_dpp v0, v0, v0 row_half_mirror row_mask:0xf bank_mask:0xf
	s_nop 1
	v_max_f32_dpp v0, v0, v0 row_mirror row_mask:0xf bank_mask:0xf
	s_nop 1
	v_max_f32_dpp v0, v0, v0 row_bcast:15 row_mask:0xa bank_mask:0xf
	s_nop 1
	v_max_f32_dpp v0, v0, v0 row_bcast:31 row_mask:0xc bank_mask:0xf
	s_nop 1
	v_readlane_b32 s100, v0, 63
	s_nop 3
	v_mov_b32_e32 v0, s100
	v_mov_b32_e32 v3, s100
	s_waitcnt lgkmcnt(0)
	v_max3_f32 v0, v0, v3, s64
	v_div_scale_f32 v3, s[2:3], v0, v0, s65
	v_rcp_f32_e32 v4, v3
	v_div_scale_f32 v5, vcc, s65, v0, s65
	v_fma_f32 v6, -v3, v4, 1.0
	v_fmac_f32_e32 v4, v6, v4
	v_mul_f32_e32 v6, v5, v4
	v_fma_f32 v7, -v3, v6, v5
	v_fmac_f32_e32 v6, v7, v4
	v_fma_f32 v3, -v3, v6, v5
	v_div_fmas_f32 v3, v3, v4, v6
	v_div_fixup_f32 v0, v3, v0, s65
	v_min_f32_e32 v0, 0x5d5e0b6b, v0
	v_and_b32_e32 v0, 0x7f800000, v0
	v_fma_mixlo_f16 v1, v1, v0, 0
	v_fma_mixlo_f16 v2, v2, v0, 0
	v_mul_u32_u24_sdwa v1, v1, s66 dst_sel:DWORD dst_unused:UNUSED_PAD src0_sel:WORD_0 src1_sel:DWORD
	v_mul_u32_u24_sdwa v2, v2, s66 dst_sel:DWORD dst_unused:UNUSED_PAD src0_sel:WORD_0 src1_sel:DWORD
	ds_write2st64_b32 v12, v1, v2 offset0:28 offset1:29
	s_and_saveexec_b64 s[2:3], s[34:35]
	s_cbranch_execz .LBB0_1239
	v_div_scale_f32 v1, s[4:5], v0, v0, 1.0
	v_rcp_f32_e32 v2, v1
	v_div_scale_f32 v3, vcc, 1.0, v0, 1.0
	v_fma_f32 v4, -v1, v2, 1.0
	v_fmac_f32_e32 v2, v4, v2
	v_mul_f32_e32 v4, v3, v2
	v_fma_f32 v5, -v1, v4, v3
	v_fmac_f32_e32 v4, v5, v2
	v_fma_f32 v1, -v1, v4, v3
	v_div_fmas_f32 v1, v1, v2, v4
	v_div_fixup_f32 v0, v1, v0, 1.0
	v_mov_b32_e32 v1, s83
	ds_write_b32 v1, v0 offset:10300

; #define GAS __attribute__((address_space(1)))
; __device__ __forceinline__ float frsq(float x) { return __builtin_amdgcn_rsqf(x); }
; __device__ __forceinline__ void expert_phase(const Frame& F, int l, int xcc, LAS unsigned char* wl, const LAS unsigned char* zb) {
;     ...
;         if (l + 1 < DEPTH) {
;             float* RSTD = (float*)(F.ws + WS_RSTD);
; #pragma unroll
;             for (int k = 0; k < 8; ++k) { const float r1 = frsq(wave_sum(SQ[k * 64 + lane]) * (1.f / D) + EPS); if (lane == 0) *(GAS float*)(RSTD + tok(k)) = r1; }
;         }
.LBB0_1249:
	s_waitcnt vmcnt(0)
	s_and_b64 vcc, exec, s[20:21]
	s_cbranch_vccz .LBB0_1124
	ds_read_b32 v0, v201 offset:8192
	s_waitcnt lgkmcnt(0)
	s_waitcnt lgkmcnt(0)
	s_nop 1
	v_add_f32_dpp v0, v0, v0 quad_perm:[1,0,3,2] row_mask:0xf bank_mask:0xf
	s_nop 1
	v_add_f32_dpp v0, v0, v0 quad_perm:[2,3,0,1] row_mask:0xf bank_mask:0xf
	s_nop 1
	v_add_f32_dpp v0, v0, v0 row_half_mirror row_mask:0xf bank_mask:0xf
	s_nop 1
	v_add_f32_dpp v0, v0, v0 row_mirror row_mask:0xf bank_mask:0xf
	s_nop 1
	v_add_f32_dpp v0, v0, v0 row_bcast:15 row_mask:0xa bank_mask:0xf
	s_nop 1
	v_add_f32_dpp v0, v0, v0 row_bcast:31 row_mask:0xc bank_mask:0xf
	s_nop 1
	v_readlane_b32 s100, v0, 63
	s_nop 3
	v_mov_b32_e32 v0, s100
	v_mov_b32_e32 v1, 0
	s_and_saveexec_b64 s[2:3], s[34:35]
	s_cbranch_execz .LBB0_1252
	s_waitcnt lgkmcnt(0)
	v_add_f32_e32 v0, v0, v1
	v_fmamk_f32 v0, v0, 0x3a000000, v214
	v_rsq_f32_e32 v0, v0
	s_lshl_b64 s[4:5], s[26:27], 2
	v_readlane_b32 s8, v250, 22
	v_readlane_b32 s9, v250, 23
	s_add_u32 s4, s8, s4
	s_addc_u32 s5, s9, s5
	global_store_dword v185, v0, s[4:5]
.LBB0_1252:
	s_or_b64 exec, exec, s[2:3]
	ds_read_b32 v0, v201 offset:8448
	s_waitcnt lgkmcnt(0)
	s_waitcnt lgkmcnt(0)
	s_nop 1
	v_add_f32_dpp v0, v0, v0 quad_perm:[1,0,3,2] row_mask:0xf bank_mask:0xf
	s_nop 1
	v_add_f32_dpp v0, v0, v0 quad_perm:[2,3,0,1] row_mask:0xf bank_mask:0xf
	s_nop 1
	v_add_f32_dpp v0, v0, v0 row_half_mirror row_mask:0xf bank_mask:0xf
	s_nop 1
	v_add_f32_dpp v0, v0, v0 row_mirror row_mask:0xf bank_mask:0xf
	s_nop 1
	v_add_f32_dpp v0, v0, v0 row_bcast:15 row_mask:0xa bank_mask:0xf
	s_nop 1
	v_add_f32_dpp v0, v0, v0 row_bcast:31 row_mask:0xc bank_mask:0xf
	s_nop 1
	v_readlane_b32 s100, v0, 63
	s_nop 3
	v_mov_b32_e32 v0, s100
	v_mov_b32_e32 v1, 0
	s_and_saveexec_b64 s[2:3], s[34:35]
	s_cbranch_execz .LBB0_1254
	s_waitcnt lgkmcnt(0)
	v_add_f32_e32 v0, v0, v1
	v_fmamk_f32 v0, v0, 0x3a000000, v214
	v_rsq_f32_e32 v0, v0
	s_lshl_b64 s[4:5], s[88:89], 2
	v_readlane_b32 s8, v250, 22
	v_readlane_b32 s9, v250, 23
	s_add_u32 s4, s8, s4
	s_addc_u32 s5, s9, s5
	global_store_dword v185, v0, s[4:5]
.LBB0_1254:
	s_or_b64 exec, exec, s[2:3]
	ds_read_b32 v0, v201 offset:8704
	s_waitcnt lgkmcnt(0)
	s_waitcnt lgkmcnt(0)
	s_nop 1
	v_add_f32_dpp v0, v0, v0 quad_perm:[1,0,3,2] row_mask:0xf bank_mask:0xf
	s_nop 1
	v_add_f32_dpp v0, v0, v0 quad_perm:[2,3,0,1] row_mask:0xf bank_mask:0xf
	s_nop 1
	v_add_f32_dpp v0, v0, v0 row_half_mirror row_mask:0xf bank_mask:0xf
	s_nop 1
	v_add_f32_dpp v0, v0, v0 row_mirror row_mask:0xf bank_mask:0xf
	s_nop 1
	v_add_f32_dpp v0, v0, v0 row_bcast:15 row_mask:0xa bank_mask:0xf
	s_nop 1
	v_add_f32_dpp v0, v0, v0 row_bcast:31 row_mask:0xc bank_mask:0xf
	s_nop 1
	v_readlane_b32 s100, v0, 63
	s_nop 3
	v_mov_b32_e32 v0, s100
	v_mov_b32_e32 v1, 0
	s_and_saveexec_b64 s[2:3], s[34:35]
	s_cbranch_execz .LBB0_1256
	s_waitcnt lgkmcnt(0)
	v_add_f32_e32 v0, v0, v1
	v_fmamk_f32 v0, v0, 0x3a000000, v214
	v_rsq_f32_e32 v0, v0
	s_lshl_b64 s[0:1], s[0:1], 2
	v_readlane_b32 s4, v250, 22
	v_readlane_b32 s5, v250, 23
	s_add_u32 s0, s4, s0
	s_addc_u32 s1, s5, s1
	global_store_dword v185, v0, s[0:1]
.LBB0_1256:
	s_or_b64 exec, exec, s[2:3]
	ds_read_b32 v0, v201 offset:8960
	s_waitcnt lgkmcnt(0)
	s_waitcnt lgkmcnt(0)
	s_nop 1
	v_add_f32_dpp v0, v0, v0 quad_perm:[1,0,3,2] row_mask:0xf bank_mask:0xf
	s_nop 1
	v_add_f32_dpp v0, v0, v0 quad_perm:[2,3,0,1] row_mask:0xf bank_mask:0xf
	s_nop 1
	v_add_f32_dpp v0, v0, v0 row_half_mirror row_mask:0xf bank_mask:0xf
	s_nop 1
	v_add_f32_dpp v0, v0, v0 row_mirror row_mask:0xf bank_mask:0xf
	s_nop 1
	v_add_f32_dpp v0, v0, v0 row_bcast:15 row_mask:0xa bank_mask:0xf
	s_nop 1
	v_add_f32_dpp v0, v0, v0 row_bcast:31 row_mask:0xc bank_mask:0xf
	s_nop 1
	v_readlane_b32 s100, v0, 63
	s_nop 3
	v_mov_b32_e32 v0, s100
	v_mov_b32_e32 v1, 0
	s_and_saveexec_b64 s[0:1], s[34:35]
	s_cbranch_execz .LBB0_1258
	s_waitcnt lgkmcnt(0)
	v_add_f32_e32 v0, v0, v1
	v_fmamk_f32 v0, v0, 0x3a000000, v214
	v_rsq_f32_e32 v0, v0
	s_lshl_b64 s[2:3], s[16:17], 2
	v_readlane_b32 s4, v250, 22
	v_readlane_b32 s5, v250, 23
	s_add_u32 s2, s4, s2
	s_addc_u32 s3, s5, s3
	global_store_dword v185, v0, s[2:3]
; #define GAS __attribute__((address_space(1)))
; __device__ __forceinline__ float frsq(float x) { return __builtin_amdgcn_rsqf(x); }
; __device__ __forceinline__ void expert_phase(const Frame& F, int l, int xcc, LAS unsigned char* wl, const LAS unsigned char* zb) {
;     ...
;         if (l + 1 < DEPTH) {
;             float* RSTD = (float*)(F.ws + WS_RSTD);
; #pragma unroll
;             for (int k = 0; k < 8; ++k) { const float r1 = frsq(wave_sum(SQ[k * 64 + lane]) * (1.f / D) + EPS); if (lane == 0) *(GAS float*)(RSTD + tok(k)) = r1; }
;         }
.LBB0_1258:
	s_or_b64 exec, exec, s[0:1]
	ds_read_b32 v0, v201 offset:9216
	s_waitcnt lgkmcnt(0)
	s_waitcnt lgkmcnt(0)
	s_nop 1
	v_add_f32_dpp v0, v0, v0 quad_perm:[1,0,3,2] row_mask:0xf bank_mask:0xf
	s_nop 1
	v_add_f32_dpp v0, v0, v0 quad_perm:[2,3,0,1] row_mask:0xf bank_mask:0xf
	s_nop 1
	v_add_f32_dpp v0, v0, v0 row_half_mirror row_mask:0xf bank_mask:0xf
	s_nop 1
	v_add_f32_dpp v0, v0, v0 row_mirror row_mask:0xf bank_mask:0xf
	s_nop 1
	v_add_f32_dpp v0, v0, v0 row_bcast:15 row_mask:0xa bank_mask:0xf
	s_nop 1
	v_add_f32_dpp v0, v0, v0 row_bcast:31 row_mask:0xc bank_mask:0xf
	s_nop 1
	v_readlane_b32 s100, v0, 63
	s_nop 3
	v_mov_b32_e32 v0, s100
	v_mov_b32_e32 v1, 0
	s_and_saveexec_b64 s[0:1], s[34:35]
	s_cbranch_execz .LBB0_1260
	s_waitcnt lgkmcnt(0)
	v_add_f32_e32 v0, v0, v1
	v_fmamk_f32 v0, v0, 0x3a000000, v214
	v_rsq_f32_e32 v0, v0
	s_lshl_b64 s[2:3], s[14:15], 2
	v_readlane_b32 s4, v250, 22
	v_readlane_b32 s5, v250, 23
	s_add_u32 s2, s4, s2
	s_addc_u32 s3, s5, s3
	global_store_dword v185, v0, s[2:3]
.LBB0_1260:
	s_or_b64 exec, exec, s[0:1]
	ds_read_b32 v0, v201 offset:9472
	s_waitcnt lgkmcnt(0)
	s_waitcnt lgkmcnt(0)
	s_nop 1
	v_add_f32_dpp v0, v0, v0 quad_perm:[1,0,3,2] row_mask:0xf bank_mask:0xf
	s_nop 1
	v_add_f32_dpp v0, v0, v0 quad_perm:[2,3,0,1] row_mask:0xf bank_mask:0xf
	s_nop 1
	v_add_f32_dpp v0, v0, v0 row_half_mirror row_mask:0xf bank_mask:0xf
	s_nop 1
	v_add_f32_dpp v0, v0, v0 row_mirror row_mask:0xf bank_mask:0xf
	s_nop 1
	v_add_f32_dpp v0, v0, v0 row_bcast:15 row_mask:0xa bank_mask:0xf
	s_nop 1
	v_add_f32_dpp v0, v0, v0 row_bcast:31 row_mask:0xc bank_mask:0xf
	s_nop 1
	v_readlane_b32 s100, v0, 63
	s_nop 3
	v_mov_b32_e32 v0, s100
	v_mov_b32_e32 v1, 0
	s_and_saveexec_b64 s[0:1], s[34:35]
	s_cbranch_execz .LBB0_1262
	s_waitcnt lgkmcnt(0)
	v_add_f32_e32 v0, v0, v1
	v_fmamk_f32 v0, v0, 0x3a000000, v214
	v_rsq_f32_e32 v0, v0
	s_lshl_b64 s[2:3], s[12:13], 2
	v_readlane_b32 s4, v250, 22
	v_readlane_b32 s5, v250, 23
	s_add_u32 s2, s4, s2
	s_addc_u32 s3, s5, s3
	global_store_dword v185, v0, s[2:3]
.LBB0_1262:
	s_or_b64 exec, exec, s[0:1]
	ds_read_b32 v0, v201 offset:9728
	s_waitcnt lgkmcnt(0)
	s_waitcnt lgkmcnt(0)
	s_nop 1
	v_add_f32_dpp v0, v0, v0 quad_perm:[1,0,3,2] row_mask:0xf bank_mask:0xf
	s_nop 1
	v_add_f32_dpp v0, v0, v0 quad_perm:[2,3,0,1] row_mask:0xf bank_mask:0xf
	s_nop 1
	v_add_f32_dpp v0, v0, v0 row_half_mirror row_mask:0xf bank_mask:0xf
	s_nop 1
	v_add_f32_dpp v0, v0, v0 row_mirror row_mask:0xf bank_mask:0xf
	s_nop 1
	v_add_f32_dpp v0, v0, v0 row_bcast:15 row_mask:0xa bank_mask:0xf
	s_nop 1
	v_add_f32_dpp v0, v0, v0 row_bcast:31 row_mask:0xc bank_mask:0xf
	s_nop 1
	v_readlane_b32 s100, v0, 63
	s_nop 3
	v_mov_b32_e32 v0, s100
	v_mov_b32_e32 v1, 0
	s_and_saveexec_b64 s[0:1], s[34:35]
	s_cbranch_execz .LBB0_1264
	s_waitcnt lgkmcnt(0)
	v_add_f32_e32 v0, v0, v1
	v_fmamk_f32 v0, v0, 0x3a000000, v214
	v_rsq_f32_e32 v0, v0
	s_lshl_b64 s[2:3], s[94:95], 2
	v_readlane_b32 s4, v250, 22
	v_readlane_b32 s5, v250, 23
	s_add_u32 s2, s4, s2
	s_addc_u32 s3, s5, s3
	global_store_dword v185, v0, s[2:3]
.LBB0_1264:
	s_or_b64 exec, exec, s[0:1]
	ds_read_b32 v0, v201 offset:9984
	s_waitcnt lgkmcnt(0)
	s_waitcnt lgkmcnt(0)
	s_nop 1
	v_add_f32_dpp v0, v0, v0 quad_perm:[1,0,3,2] row_mask:0xf bank_mask:0xf
	s_nop 1
	v_add_f32_dpp v0, v0, v0 quad_perm:[2,3,0,1] row_mask:0xf bank_mask:0xf
	s_nop 1
	v_add_f32_dpp v0, v0, v0 row_half_mirror row_mask:0xf bank_mask:0xf
	s_nop 1
	v_add_f32_dpp v0, v0, v0 row_mirror row_mask:0xf bank_mask:0xf
	s_nop 1
	v_add_f32_dpp v0, v0, v0 row_bcast:15 row_mask:0xa bank_mask:0xf
	s_nop 1
	v_add_f32_dpp v0, v0, v0 row_bcast:31 row_mask:0xc bank_mask:0xf
	s_nop 1
	v_readlane_b32 s100, v0, 63
	s_nop 3
	v_mov_b32_e32 v0, s100
	v_mov_b32_e32 v1, 0
	s_and_saveexec_b64 s[0:1], s[34:35]
	s_cbranch_execz .LBB0_1123
	s_waitcnt lgkmcnt(0)
	v_add_f32_e32 v0, v0, v1
	v_fmamk_f32 v0, v0, 0x3a000000, v214
	v_rsq_f32_e32 v0, v0
	s_lshl_b64 s[2:3], s[6:7], 2
	v_readlane_b32 s4, v250, 22
	v_readlane_b32 s5, v250, 23
	s_add_u32 s2, s4, s2
	s_addc_u32 s3, s5, s3
	global_store_dword v185, v0, s[2:3]
	s_branch .LBB0_1123
